# baseline (speedup 1.0000x reference)
.Lrot1_done:
	s_lshl_b64 s[0:1], s[18:19], 24
	ds_read_b128 v[180:183], v210 offset:0
	ds_read_b128 v[184:187], v210 offset:0x800
	ds_read_b128 v[188:191], v210 offset:0x1000
	ds_read_b128 v[192:195], v210 offset:0x1800
	ds_read_b128 v[212:215], v209 offset:0
	ds_read_b128 v[216:219], v209 offset:0x800
	ds_read_b128 v[220:223], v209 offset:0x1000
	s_waitcnt lgkmcnt(0)
	s_add_u32 s0, s10, s0
	s_addc_u32 s18, s11, s1
	s_lshl_b32 s19, s24, 1
	s_mov_b32 s1, 0
	s_add_u32 s0, s0, s19
	s_waitcnt lgkmcnt(2)
	s_addc_u32 s20, s18, 0
	v_mfma_f32_16x16x32_bf16 v[174:177], v[180:183], v[212:215], v[174:177]
	v_mfma_f32_16x16x32_bf16 v[170:173], v[184:187], v[212:215], v[170:173]
	v_mfma_f32_16x16x32_bf16 v[166:169], v[188:191], v[212:215], v[166:169]
	v_mfma_f32_16x16x32_bf16 v[162:165], v[192:195], v[212:215], v[162:165]
	ds_read_b128 v[212:215], v209 offset:0x1800
	s_waitcnt lgkmcnt(2)
	v_mfma_f32_16x16x32_bf16 v[158:161], v[180:183], v[216:219], v[158:161]
	v_mfma_f32_16x16x32_bf16 v[154:157], v[184:187], v[216:219], v[154:157]
	v_mfma_f32_16x16x32_bf16 v[150:153], v[188:191], v[216:219], v[150:153]
	v_mfma_f32_16x16x32_bf16 v[146:149], v[192:195], v[216:219], v[146:149]
	ds_read_b128 v[216:219], v209 offset:0x2000
	s_waitcnt lgkmcnt(2)
	v_mfma_f32_16x16x32_bf16 v[142:145], v[180:183], v[220:223], v[142:145]
	v_mfma_f32_16x16x32_bf16 v[138:141], v[184:187], v[220:223], v[138:141]
	v_mfma_f32_16x16x32_bf16 v[134:137], v[188:191], v[220:223], v[134:137]
	v_mfma_f32_16x16x32_bf16 v[130:133], v[192:195], v[220:223], v[130:133]
	ds_read_b128 v[220:223], v209 offset:0x2800
	s_waitcnt lgkmcnt(2)
	v_mfma_f32_16x16x32_bf16 v[126:129], v[180:183], v[212:215], v[126:129]
	v_mfma_f32_16x16x32_bf16 v[122:125], v[184:187], v[212:215], v[122:125]
	v_mfma_f32_16x16x32_bf16 v[118:121], v[188:191], v[212:215], v[118:121]
	v_mfma_f32_16x16x32_bf16 v[114:117], v[192:195], v[212:215], v[114:117]
	ds_read_b128 v[212:215], v209 offset:0x3000
	s_waitcnt lgkmcnt(2)
	v_mfma_f32_16x16x32_bf16 v[110:113], v[180:183], v[216:219], v[110:113]
	v_mfma_f32_16x16x32_bf16 v[106:109], v[184:187], v[216:219], v[106:109]
	v_mfma_f32_16x16x32_bf16 v[102:105], v[188:191], v[216:219], v[102:105]
	v_mfma_f32_16x16x32_bf16 v[98:101], v[192:195], v[216:219], v[98:101]
	ds_read_b128 v[216:219], v209 offset:0x3800
	s_waitcnt lgkmcnt(2)
	v_mfma_f32_16x16x32_bf16 v[94:97], v[180:183], v[220:223], v[94:97]
	v_mfma_f32_16x16x32_bf16 v[90:93], v[184:187], v[220:223], v[90:93]
	v_mfma_f32_16x16x32_bf16 v[86:89], v[188:191], v[220:223], v[86:89]
	v_mfma_f32_16x16x32_bf16 v[82:85], v[192:195], v[220:223], v[82:85]
	s_waitcnt lgkmcnt(1)
	v_mfma_f32_16x16x32_bf16 v[78:81], v[180:183], v[212:215], v[78:81]
	v_mfma_f32_16x16x32_bf16 v[74:77], v[184:187], v[212:215], v[74:77]
	v_mfma_f32_16x16x32_bf16 v[70:73], v[188:191], v[212:215], v[70:73]
	v_mfma_f32_16x16x32_bf16 v[66:69], v[192:195], v[212:215], v[66:69]
	s_waitcnt lgkmcnt(0)
	v_mfma_f32_16x16x32_bf16 v[62:65], v[180:183], v[216:219], v[62:65]
	v_mfma_f32_16x16x32_bf16 v[58:61], v[184:187], v[216:219], v[58:61]
	v_mfma_f32_16x16x32_bf16 v[54:57], v[188:191], v[216:219], v[54:57]
	v_mfma_f32_16x16x32_bf16 v[50:53], v[192:195], v[216:219], v[50:53]
	s_add_i32 s18, 0, 0x10000
	s_waitcnt vmcnt(10)
	v_cvt_pk_bf16_f32 v46, v46, v47
	v_cvt_pk_bf16_f32 v47, v48, v49
	v_cvt_pk_bf16_f32 v48, v42, v43
	v_add_u32_e32 v42, s18, v208
	s_waitcnt vmcnt(8)
	v_cvt_pk_bf16_f32 v38, v38, v39
	v_cvt_pk_bf16_f32 v39, v40, v41
	v_cvt_pk_bf16_f32 v40, v34, v35
	v_add_u32_e32 v34, s18, v205
	s_add_i32 s19, 0, 0x18000
	v_cvt_pk_bf16_f32 v49, v44, v45
	ds_write_b128 v42, v[46:49]
	v_cvt_pk_bf16_f32 v41, v36, v37
	ds_write_b128 v34, v[38:41]
	v_add_u32_e32 v34, s19, v206
	s_waitcnt vmcnt(7)
	ds_write_b128 v34, v[30:33]
	v_add_u32_e32 v30, s19, v207
	s_waitcnt vmcnt(6)
	ds_write_b128 v30, v[26:29]
	ds_read_b128 v[26:29], v210 offset:0x400
	ds_read_b128 v[30:33], v210 offset:0xc00
	ds_read_b128 v[34:37], v210 offset:0x1400
	ds_read_b128 v[38:41], v210 offset:0x1c00
	ds_read_b128 v[42:45], v209 offset:0x400
	ds_read_b128 v[46:49], v209 offset:0xc00
	ds_read_b128 v[180:183], v209 offset:0x1400
	s_waitcnt lgkmcnt(2)
	v_mfma_f32_16x16x32_bf16 v[174:177], v[26:29], v[42:45], v[174:177]
	v_mfma_f32_16x16x32_bf16 v[170:173], v[30:33], v[42:45], v[170:173]
	v_mfma_f32_16x16x32_bf16 v[166:169], v[34:37], v[42:45], v[166:169]
	v_mfma_f32_16x16x32_bf16 v[42:45], v[38:41], v[42:45], v[162:165]
	ds_read_b128 v[162:165], v209 offset:0x1c00
	s_waitcnt lgkmcnt(2)
	v_mfma_f32_16x16x32_bf16 v[158:161], v[26:29], v[46:49], v[158:161]
	v_mfma_f32_16x16x32_bf16 v[154:157], v[30:33], v[46:49], v[154:157]
	v_mfma_f32_16x16x32_bf16 v[150:153], v[34:37], v[46:49], v[150:153]
	v_mfma_f32_16x16x32_bf16 v[46:49], v[38:41], v[46:49], v[146:149]
	ds_read_b128 v[146:149], v209 offset:0x2400
	s_waitcnt lgkmcnt(2)
	v_mfma_f32_16x16x32_bf16 v[142:145], v[26:29], v[180:183], v[142:145]
	v_mfma_f32_16x16x32_bf16 v[138:141], v[30:33], v[180:183], v[138:141]
	v_mfma_f32_16x16x32_bf16 v[134:137], v[34:37], v[180:183], v[134:137]
	v_mfma_f32_16x16x32_bf16 v[130:133], v[38:41], v[180:183], v[130:133]
	ds_read_b128 v[180:183], v209 offset:0x2c00
	s_waitcnt lgkmcnt(2)
	v_mfma_f32_16x16x32_bf16 v[126:129], v[26:29], v[162:165], v[126:129]
	v_mfma_f32_16x16x32_bf16 v[122:125], v[30:33], v[162:165], v[122:125]
	v_mfma_f32_16x16x32_bf16 v[118:121], v[34:37], v[162:165], v[118:121]
	v_mfma_f32_16x16x32_bf16 v[114:117], v[38:41], v[162:165], v[114:117]
	ds_read_b128 v[162:165], v209 offset:0x3400
	s_waitcnt lgkmcnt(2)
	v_mfma_f32_16x16x32_bf16 v[110:113], v[26:29], v[146:149], v[110:113]
	v_mfma_f32_16x16x32_bf16 v[106:109], v[30:33], v[146:149], v[106:109]
	v_mfma_f32_16x16x32_bf16 v[102:105], v[34:37], v[146:149], v[102:105]
	v_mfma_f32_16x16x32_bf16 v[98:101], v[38:41], v[146:149], v[98:101]
	ds_read_b128 v[146:149], v209 offset:0x3c00
	s_waitcnt lgkmcnt(2)
	v_mfma_f32_16x16x32_bf16 v[94:97], v[26:29], v[180:183], v[94:97]
	v_mfma_f32_16x16x32_bf16 v[90:93], v[30:33], v[180:183], v[90:93]
	v_mfma_f32_16x16x32_bf16 v[86:89], v[34:37], v[180:183], v[86:89]
	v_mfma_f32_16x16x32_bf16 v[82:85], v[38:41], v[180:183], v[82:85]
	s_waitcnt lgkmcnt(1)
	v_mfma_f32_16x16x32_bf16 v[78:81], v[26:29], v[162:165], v[78:81]
	v_mfma_f32_16x16x32_bf16 v[74:77], v[30:33], v[162:165], v[74:77]
	v_mfma_f32_16x16x32_bf16 v[70:73], v[34:37], v[162:165], v[70:73]
	v_mfma_f32_16x16x32_bf16 v[66:69], v[38:41], v[162:165], v[66:69]
	s_waitcnt lgkmcnt(0)
	v_mfma_f32_16x16x32_bf16 v[26:29], v[26:29], v[146:149], v[62:65]
	v_mfma_f32_16x16x32_bf16 v[30:33], v[30:33], v[146:149], v[58:61]
	v_mfma_f32_16x16x32_bf16 v[34:37], v[34:37], v[146:149], v[54:57]
	v_mfma_f32_16x16x32_bf16 v[38:41], v[38:41], v[146:149], v[50:53]
	s_waitcnt vmcnt(4)
	v_cvt_pk_bf16_f32 v22, v22, v23
	v_cvt_pk_bf16_f32 v23, v24, v25
	v_cvt_pk_bf16_f32 v24, v6, v7
	v_cvt_pk_bf16_f32 v25, v8, v9
	v_add_u32_e32 v6, s18, v204
	s_waitcnt vmcnt(3)
	v_cvt_pk_bf16_f32 v8, v2, v3
	v_add_u32_e32 v2, s18, v201
	ds_write_b128 v6, v[22:25]
	s_waitcnt vmcnt(2)
	v_cvt_pk_bf16_f32 v6, v10, v11
	v_cvt_pk_bf16_f32 v7, v12, v13
	v_cvt_pk_bf16_f32 v9, v4, v5
	ds_write_b128 v2, v[6:9]
	v_add_u32_e32 v2, s19, v202
	s_waitcnt vmcnt(1)
	ds_write_b128 v2, v[18:21]
	v_add_u32_e32 v2, s19, v203
	s_waitcnt vmcnt(0)
	ds_write_b128 v2, v[14:17]
	s_waitcnt lgkmcnt(0)
	s_barrier
	v_add_u32_e32 v178, 0x10000, v209
	v_add_u32_e32 v196, 0x10000, v210
	ds_read_b128 v[2:5], v196 offset:0
	ds_read_b128 v[6:9], v196 offset:0x800
	ds_read_b128 v[10:13], v196 offset:0x1000
	ds_read_b128 v[14:17], v196 offset:0x1800
	ds_read_b128 v[18:21], v178 offset:0
	s_and_b64 s[16:17], s[16:17], exec
	ds_read_b128 v[22:25], v178 offset:0x800
	ds_read_b128 v[50:53], v178 offset:0x1000
	s_waitcnt lgkmcnt(2)
	s_cselect_b32 s5, s5, s7
	s_cselect_b32 s4, s4, s6
	s_lshl_b32 s6, s3, 10
	v_mfma_f32_16x16x32_bf16 v[54:57], v[2:5], v[18:21], v[174:177]
	s_add_u32 s6, s4, s6
	s_addc_u32 s7, s5, 0
	s_lshl_b32 s3, s3, 9
	v_mfma_f32_16x16x32_bf16 v[58:61], v[6:9], v[18:21], v[170:173]
	s_add_u32 s4, s0, s3
	s_addc_u32 s5, s20, 0
	v_mfma_f32_16x16x32_bf16 v[62:65], v[10:13], v[18:21], v[166:169]
	v_mfma_f32_16x16x32_bf16 v[18:21], v[14:17], v[18:21], v[42:45]
	ds_read_b128 v[42:45], v178 offset:0x1800
	s_waitcnt lgkmcnt(2)
	v_mfma_f32_16x16x32_bf16 v[146:149], v[2:5], v[22:25], v[158:161]
	v_mfma_f32_16x16x32_bf16 v[154:157], v[6:9], v[22:25], v[154:157]
	v_mfma_f32_16x16x32_bf16 v[150:153], v[10:13], v[22:25], v[150:153]
	v_mfma_f32_16x16x32_bf16 v[22:25], v[14:17], v[22:25], v[46:49]
	ds_read_b128 v[46:49], v178 offset:0x2000
	s_waitcnt lgkmcnt(2)
	v_mfma_f32_16x16x32_bf16 v[142:145], v[2:5], v[50:53], v[142:145]
	v_mfma_f32_16x16x32_bf16 v[138:141], v[6:9], v[50:53], v[138:141]
	v_mfma_f32_16x16x32_bf16 v[134:137], v[10:13], v[50:53], v[134:137]
	v_mfma_f32_16x16x32_bf16 v[50:53], v[14:17], v[50:53], v[130:133]
	ds_read_b128 v[130:133], v178 offset:0x2800
	s_waitcnt lgkmcnt(2)
	v_mfma_f32_16x16x32_bf16 v[126:129], v[2:5], v[42:45], v[126:129]
	v_mfma_f32_16x16x32_bf16 v[122:125], v[6:9], v[42:45], v[122:125]
	v_mfma_f32_16x16x32_bf16 v[118:121], v[10:13], v[42:45], v[118:121]
	v_mfma_f32_16x16x32_bf16 v[42:45], v[14:17], v[42:45], v[114:117]
	ds_read_b128 v[114:117], v178 offset:0x3000
	s_waitcnt lgkmcnt(2)
	v_mfma_f32_16x16x32_bf16 v[110:113], v[2:5], v[46:49], v[110:113]
	v_mfma_f32_16x16x32_bf16 v[106:109], v[6:9], v[46:49], v[106:109]
	v_mfma_f32_16x16x32_bf16 v[102:105], v[10:13], v[46:49], v[102:105]
	v_mfma_f32_16x16x32_bf16 v[98:101], v[14:17], v[46:49], v[98:101]
	ds_read_b128 v[46:49], v178 offset:0x3800
	s_waitcnt lgkmcnt(2)
	v_mfma_f32_16x16x32_bf16 v[158:161], v[2:5], v[130:133], v[94:97]
	v_mfma_f32_16x16x32_bf16 v[162:165], v[6:9], v[130:133], v[90:93]
	v_mfma_f32_16x16x32_bf16 v[166:169], v[10:13], v[130:133], v[86:89]
	v_mfma_f32_16x16x32_bf16 v[130:133], v[14:17], v[130:133], v[82:85]
	s_waitcnt lgkmcnt(1)
	v_mfma_f32_16x16x32_bf16 v[66:69], v[14:17], v[114:117], v[66:69]
	v_mfma_f32_16x16x32_bf16 v[170:173], v[2:5], v[114:117], v[78:81]
	v_mfma_f32_16x16x32_bf16 v[174:177], v[6:9], v[114:117], v[74:77]
	v_mfma_f32_16x16x32_bf16 v[180:183], v[10:13], v[114:117], v[70:73]
	s_waitcnt lgkmcnt(0)
	v_mfma_f32_16x16x32_bf16 v[2:5], v[2:5], v[46:49], v[26:29]
	v_mfma_f32_16x16x32_bf16 v[114:117], v[6:9], v[46:49], v[30:33]
	v_mfma_f32_16x16x32_bf16 v[34:37], v[10:13], v[46:49], v[34:37]
	v_mfma_f32_16x16x32_bf16 v[184:187], v[14:17], v[46:49], v[38:41]
	ds_read_b128 v[188:191], v196 offset:0x400
	ds_read_b128 v[192:195], v196 offset:0xc00
	ds_read_b128 v[202:205], v196 offset:0x1400
	ds_read_b128 v[206:209], v196 offset:0x1c00
	ds_read_b128 v[6:9], v178 offset:0x400
	ds_read_b128 v[10:13], v178 offset:0xc00
	ds_read_b128 v[14:17], v178 offset:0x1400
	s_waitcnt lgkmcnt(2)
	v_mfma_f32_16x16x32_bf16 v[94:97], v[192:195], v[6:9], v[58:61]
	v_mfma_f32_16x16x32_bf16 v[62:65], v[202:205], v[6:9], v[62:65]
	v_mfma_f32_16x16x32_bf16 v[30:33], v[206:209], v[6:9], v[18:21]
	v_mfma_f32_16x16x32_bf16 v[210:213], v[188:191], v[6:9], v[54:57]
	ds_read_b128 v[6:9], v178 offset:0x1c00
	s_waitcnt lgkmcnt(2)
	v_mfma_f32_16x16x32_bf16 v[90:93], v[192:195], v[10:13], v[154:157]
	v_mfma_f32_16x16x32_bf16 v[58:61], v[202:205], v[10:13], v[150:153]
	v_mfma_f32_16x16x32_bf16 v[26:29], v[206:209], v[10:13], v[22:25]
	v_mfma_f32_16x16x32_bf16 v[146:149], v[188:191], v[10:13], v[146:149]
	ds_read_b128 v[10:13], v178 offset:0x2400
	s_waitcnt lgkmcnt(2)
	v_mfma_f32_16x16x32_bf16 v[86:89], v[192:195], v[14:17], v[138:141]
	v_mfma_f32_16x16x32_bf16 v[54:57], v[202:205], v[14:17], v[134:137]
	v_mfma_f32_16x16x32_bf16 v[22:25], v[206:209], v[14:17], v[50:53]
	v_mfma_f32_16x16x32_bf16 v[142:145], v[188:191], v[14:17], v[142:145]
	ds_read_b128 v[38:41], v178 offset:0x2c00
	s_waitcnt lgkmcnt(2)
	v_mfma_f32_16x16x32_bf16 v[126:129], v[188:191], v[6:9], v[126:129]
	v_mfma_f32_16x16x32_bf16 v[82:85], v[192:195], v[6:9], v[122:125]
	v_mfma_f32_16x16x32_bf16 v[50:53], v[202:205], v[6:9], v[118:121]
	v_mfma_f32_16x16x32_bf16 v[18:21], v[206:209], v[6:9], v[42:45]
	ds_read_b128 v[6:9], v178 offset:0x3400
	s_waitcnt lgkmcnt(2)
	v_mfma_f32_16x16x32_bf16 v[110:113], v[188:191], v[10:13], v[110:113]
	v_mfma_f32_16x16x32_bf16 v[78:81], v[192:195], v[10:13], v[106:109]
	v_mfma_f32_16x16x32_bf16 v[46:49], v[202:205], v[10:13], v[102:105]
	v_mfma_f32_16x16x32_bf16 v[14:17], v[206:209], v[10:13], v[98:101]
	ds_read_b128 v[98:101], v178 offset:0x3c00
	s_waitcnt lgkmcnt(2)
	v_mfma_f32_16x16x32_bf16 v[106:109], v[188:191], v[38:41], v[158:161]
	v_mfma_f32_16x16x32_bf16 v[74:77], v[192:195], v[38:41], v[162:165]
	v_mfma_f32_16x16x32_bf16 v[42:45], v[202:205], v[38:41], v[166:169]
	v_mfma_f32_16x16x32_bf16 v[10:13], v[206:209], v[38:41], v[130:133]
	s_waitcnt lgkmcnt(1)
	v_mfma_f32_16x16x32_bf16 v[118:121], v[188:191], v[6:9], v[170:173]
	v_mfma_f32_16x16x32_bf16 v[70:73], v[192:195], v[6:9], v[174:177]
	v_mfma_f32_16x16x32_bf16 v[38:41], v[202:205], v[6:9], v[180:183]
	v_mfma_f32_16x16x32_bf16 v[6:9], v[206:209], v[6:9], v[66:69]
	s_waitcnt lgkmcnt(0)
	v_mfma_f32_16x16x32_bf16 v[122:125], v[188:191], v[98:101], v[2:5]
	v_mfma_f32_16x16x32_bf16 v[66:69], v[192:195], v[98:101], v[114:117]
	v_mfma_f32_16x16x32_bf16 v[34:37], v[202:205], v[98:101], v[34:37]
	v_mfma_f32_16x16x32_bf16 v[2:5], v[206:209], v[98:101], v[184:187]
	v_lshrrev_b32_e32 v98, 2, v199
	v_and_b32_e32 v98, 12, v98
	v_lshl_or_b32 v104, v200, 6, v98
	v_lshlrev_b32_e32 v105, 2, v104
	s_waitcnt lgkmcnt(0)
	s_barrier
	global_load_dwordx4 v[114:117], v105, s[6:7]
	v_lshrrev_b32_e32 v98, 1, v199
	v_lshlrev_b32_e32 v99, 16, v198
	v_lshlrev_b32_e32 v100, 9, v179
	v_and_b32_e32 v102, 8, v98
	v_lshrrev_b32_e32 v98, 3, v104
	v_add3_u32 v103, 0, v99, v100
	v_xor_b32_e32 v130, v98, v179
	v_bitop3_b32 v131, v98, v179, 16 bitop3:0x1e
	global_load_dwordx4 v[98:101], v105, s[6:7] offset:64
	v_lshlrev_b32_e32 v130, 4, v130
	v_lshlrev_b32_e32 v131, 4, v131
	v_add3_u32 v130, v103, v130, v102
	v_add3_u32 v131, v103, v131, v102
	s_movk_i32 s0, 0x200
	s_waitcnt vmcnt(1)
	v_add_f32_e32 v132, v210, v114
	v_add_f32_e32 v133, v211, v115
	v_add_f32_e32 v134, v212, v116
	v_add_f32_e32 v135, v213, v117
	v_add_f32_e32 v140, v142, v114
	v_add_f32_e32 v141, v143, v115
	v_add_f32_e32 v142, v144, v116
	v_add_f32_e32 v143, v145, v117
	v_add_f32_e32 v110, v110, v114
	v_add_f32_e32 v111, v111, v115
	v_add_f32_e32 v106, v106, v114
	v_add_f32_e32 v107, v107, v115
	v_add_f32_e32 v136, v146, v114
	v_add_f32_e32 v137, v147, v115
	v_add_f32_e32 v138, v148, v116
	v_add_f32_e32 v139, v149, v117
	v_add_f32_e32 v126, v126, v114
	v_add_f32_e32 v127, v127, v115
	v_add_f32_e32 v128, v128, v116
	v_add_f32_e32 v129, v129, v117
	v_add_f32_e32 v112, v112, v116
	v_add_f32_e32 v113, v113, v117
	v_add_f32_e32 v108, v108, v116
	v_add_f32_e32 v109, v109, v117
	v_max_f32_e32 v132, 0, v132
	v_max_f32_e32 v133, 0, v133
	v_max_f32_e32 v134, 0, v134
	v_max_f32_e32 v135, 0, v135
	v_max_f32_e32 v140, 0, v140
	v_max_f32_e32 v141, 0, v141
	v_max_f32_e32 v142, 0, v142
	v_max_f32_e32 v143, 0, v143
	v_max_f32_e32 v144, 0, v110
	v_max_f32_e32 v145, 0, v111
	v_max_f32_e32 v148, 0, v106
	v_max_f32_e32 v149, 0, v107
	v_cvt_pk_bf16_f32 v106, v132, v133
	v_cvt_pk_bf16_f32 v107, v134, v135
	v_cvt_pk_bf16_f32 v110, v140, v141
	v_cvt_pk_bf16_f32 v111, v142, v143
	v_add_f32_e32 v118, v118, v114
	v_add_f32_e32 v119, v119, v115
	v_max_f32_e32 v136, 0, v136
	v_max_f32_e32 v137, 0, v137
	v_max_f32_e32 v138, 0, v138
	v_max_f32_e32 v139, 0, v139
	v_max_f32_e32 v126, 0, v126
	v_max_f32_e32 v127, 0, v127
	v_max_f32_e32 v128, 0, v128
	v_max_f32_e32 v129, 0, v129
	v_max_f32_e32 v146, 0, v112
	v_max_f32_e32 v147, 0, v113
	v_max_f32_e32 v150, 0, v108
	v_max_f32_e32 v151, 0, v109
	v_cvt_pk_bf16_f32 v108, v136, v137
	v_cvt_pk_bf16_f32 v109, v138, v139
	v_cvt_pk_bf16_f32 v112, v126, v127
	v_cvt_pk_bf16_f32 v113, v128, v129
	ds_write2st64_b64 v130, v[106:107], v[110:111] offset1:32
	ds_write2st64_b64 v131, v[108:109], v[112:113] offset0:16 offset1:48
	v_add_f32_e32 v106, v121, v117
	v_add_f32_e32 v120, v120, v116
	v_max_f32_e32 v152, 0, v118
	v_max_f32_e32 v153, 0, v119
	v_max_f32_e32 v107, 0, v106
	v_cvt_pk_bf16_f32 v106, v152, v153
	v_max_f32_e32 v120, 0, v120
	v_cvt_pk_bf16_f32 v118, v144, v145
	v_cvt_pk_bf16_f32 v119, v146, v147
	v_cvt_pk_bf16_f32 v107, v120, v107
	ds_write2st64_b64 v130, v[118:119], v[106:107] offset0:64 offset1:96
	v_add_f32_e32 v106, v122, v114
	v_max_f32_e32 v106, 0, v106
	v_add_f32_e32 v107, v123, v115
	v_max_f32_e32 v107, 0, v107
	v_add_f32_e32 v108, v124, v116
	v_add_f32_e32 v109, v125, v117
	v_cvt_pk_bf16_f32 v106, v106, v107
	v_cvt_pk_bf16_f32 v126, v148, v149
	v_cvt_pk_bf16_f32 v127, v150, v151
	v_max_f32_e32 v108, 0, v108
	v_max_f32_e32 v109, 0, v109
	v_cvt_pk_bf16_f32 v107, v108, v109
	ds_write2st64_b64 v131, v[126:127], v[106:107] offset0:80 offset1:112
	v_or_b32_e32 v106, 16, v104
	s_waitcnt vmcnt(0)
	v_add_f32_e32 v94, v94, v98
	v_add_f32_e32 v95, v95, v99
	v_add_f32_e32 v96, v96, v100
	v_lshrrev_b32_e32 v106, 3, v106
	v_max_f32_e32 v94, 0, v94
	v_max_f32_e32 v95, 0, v95
	v_max_f32_e32 v96, 0, v96
	v_add_f32_e32 v97, v97, v101
	v_max_f32_e32 v97, 0, v97
	v_cvt_pk_bf16_f32 v94, v94, v95
	v_cvt_pk_bf16_f32 v95, v96, v97
	v_xor_b32_e32 v96, v106, v179
	v_lshlrev_b32_e32 v96, 4, v96
	v_add3_u32 v107, v103, v96, v102
	v_add_f32_e32 v90, v90, v98
	v_add_f32_e32 v91, v91, v99
	v_add_f32_e32 v92, v92, v100
	ds_write_b64 v107, v[94:95]
	v_max_f32_e32 v90, 0, v90
	v_max_f32_e32 v91, 0, v91
	global_load_dwordx4 v[94:97], v105, s[6:7] offset:128
	v_max_f32_e32 v92, 0, v92
	v_add_f32_e32 v93, v93, v101
	v_max_f32_e32 v93, 0, v93
	v_cvt_pk_bf16_f32 v90, v90, v91
	v_cvt_pk_bf16_f32 v91, v92, v93
	v_bitop3_b32 v92, v106, v179, 16 bitop3:0x1e
	v_add_f32_e32 v66, v66, v98
	v_lshlrev_b32_e32 v92, 4, v92
	v_add_f32_e32 v86, v86, v98
	v_add_f32_e32 v87, v87, v99
	v_add_f32_e32 v82, v82, v98
	v_add_f32_e32 v83, v83, v99
	v_add_f32_e32 v78, v78, v98
	v_add_f32_e32 v79, v79, v99
	v_add_f32_e32 v74, v74, v98
	v_add_f32_e32 v75, v75, v99
	v_add_f32_e32 v70, v70, v98
	v_add_f32_e32 v71, v71, v99
	v_max_f32_e32 v66, 0, v66
	v_add_f32_e32 v67, v67, v99
	v_add3_u32 v92, v103, v92, v102
	v_max_f32_e32 v86, 0, v86
	v_max_f32_e32 v87, 0, v87
	v_add_f32_e32 v88, v88, v100
	v_add_f32_e32 v89, v89, v101
	v_max_f32_e32 v82, 0, v82
	v_max_f32_e32 v83, 0, v83
	v_add_f32_e32 v84, v84, v100
	v_add_f32_e32 v85, v85, v101
	v_max_f32_e32 v78, 0, v78
	v_max_f32_e32 v79, 0, v79
	v_add_f32_e32 v80, v80, v100
	v_add_f32_e32 v81, v81, v101
	v_max_f32_e32 v74, 0, v74
	v_max_f32_e32 v75, 0, v75
	v_add_f32_e32 v76, v76, v100
	v_add_f32_e32 v77, v77, v101
	v_max_f32_e32 v70, 0, v70
	v_max_f32_e32 v71, 0, v71
	v_add_f32_e32 v72, v72, v100
	v_add_f32_e32 v73, v73, v101
	v_max_f32_e32 v67, 0, v67
	v_add_f32_e32 v68, v68, v100
	v_add_f32_e32 v69, v69, v101
	v_cvt_pk_bf16_f32 v66, v66, v67
	ds_write_b64 v92, v[90:91] offset:8192
	v_max_f32_e32 v88, 0, v88
	v_max_f32_e32 v89, 0, v89
	v_cvt_pk_bf16_f32 v86, v86, v87
	v_cvt_pk_bf16_f32 v87, v88, v89
	ds_write_b64 v107, v[86:87] offset:16384
	v_max_f32_e32 v84, 0, v84
	v_max_f32_e32 v85, 0, v85
	v_cvt_pk_bf16_f32 v82, v82, v83
	v_cvt_pk_bf16_f32 v83, v84, v85
	ds_write_b64 v92, v[82:83] offset:24576
	v_max_f32_e32 v80, 0, v80
	v_max_f32_e32 v81, 0, v81
	v_cvt_pk_bf16_f32 v78, v78, v79
	v_cvt_pk_bf16_f32 v79, v80, v81
	ds_write_b64 v107, v[78:79] offset:32768
	v_max_f32_e32 v76, 0, v76
	v_max_f32_e32 v77, 0, v77
	v_cvt_pk_bf16_f32 v74, v74, v75
	v_cvt_pk_bf16_f32 v75, v76, v77
	ds_write_b64 v92, v[74:75] offset:40960
	v_max_f32_e32 v72, 0, v72
	v_max_f32_e32 v73, 0, v73
	v_cvt_pk_bf16_f32 v70, v70, v71
	v_cvt_pk_bf16_f32 v71, v72, v73
	ds_write_b64 v107, v[70:71] offset:49152
	v_max_f32_e32 v68, 0, v68
	v_max_f32_e32 v69, 0, v69
	v_cvt_pk_bf16_f32 v67, v68, v69
	ds_write_b64 v92, v[66:67] offset:57344
	v_or_b32_e32 v66, 32, v104
	v_lshrrev_b32_e32 v70, 3, v66
	global_load_dwordx4 v[66:69], v105, s[6:7] offset:192
	s_waitcnt vmcnt(1)
	v_add_f32_e32 v62, v62, v94
	v_add_f32_e32 v63, v63, v95
	v_add_f32_e32 v64, v64, v96
	v_add_f32_e32 v58, v58, v94
	v_add_f32_e32 v59, v59, v95
	v_add_f32_e32 v60, v60, v96
	v_max_f32_e32 v62, 0, v62
	v_max_f32_e32 v63, 0, v63
	v_max_f32_e32 v64, 0, v64
	v_add_f32_e32 v65, v65, v97
	v_max_f32_e32 v58, 0, v58
	v_max_f32_e32 v59, 0, v59
	v_max_f32_e32 v60, 0, v60
	v_add_f32_e32 v61, v61, v97
	v_max_f32_e32 v65, 0, v65
	v_cvt_pk_bf16_f32 v62, v62, v63
	v_cvt_pk_bf16_f32 v63, v64, v65
	v_xor_b32_e32 v64, v70, v179
	v_max_f32_e32 v61, 0, v61
	v_cvt_pk_bf16_f32 v58, v58, v59
	v_cvt_pk_bf16_f32 v59, v60, v61
	v_bitop3_b32 v60, v70, v179, 16 bitop3:0x1e
	v_add_f32_e32 v34, v34, v94
	v_lshlrev_b32_e32 v64, 4, v64
	v_lshlrev_b32_e32 v60, 4, v60
	v_add_f32_e32 v54, v54, v94
	v_add_f32_e32 v55, v55, v95
	v_add_f32_e32 v50, v50, v94
	v_add_f32_e32 v51, v51, v95
	v_add_f32_e32 v46, v46, v94
	v_add_f32_e32 v47, v47, v95
	v_add_f32_e32 v42, v42, v94
	v_add_f32_e32 v43, v43, v95
	v_add_f32_e32 v38, v38, v94
	v_add_f32_e32 v39, v39, v95
	v_max_f32_e32 v34, 0, v34
	v_add_f32_e32 v35, v35, v95
	v_add3_u32 v64, v103, v64, v102
	v_add3_u32 v60, v103, v60, v102
	v_max_f32_e32 v54, 0, v54
	v_max_f32_e32 v55, 0, v55
	v_add_f32_e32 v56, v56, v96
	v_add_f32_e32 v57, v57, v97
	v_max_f32_e32 v50, 0, v50
	v_max_f32_e32 v51, 0, v51
	v_add_f32_e32 v52, v52, v96
	v_add_f32_e32 v53, v53, v97
	v_max_f32_e32 v46, 0, v46
	v_max_f32_e32 v47, 0, v47
	v_add_f32_e32 v48, v48, v96
	v_add_f32_e32 v49, v49, v97
	v_max_f32_e32 v42, 0, v42
	v_max_f32_e32 v43, 0, v43
	v_add_f32_e32 v44, v44, v96
	v_add_f32_e32 v45, v45, v97
	v_max_f32_e32 v38, 0, v38
	v_max_f32_e32 v39, 0, v39
	v_add_f32_e32 v40, v40, v96
	v_add_f32_e32 v41, v41, v97
	v_max_f32_e32 v35, 0, v35
	v_add_f32_e32 v36, v36, v96
	v_add_f32_e32 v37, v37, v97
	v_cvt_pk_bf16_f32 v34, v34, v35
	ds_write_b64 v64, v[62:63]
	ds_write_b64 v60, v[58:59] offset:8192
	v_max_f32_e32 v56, 0, v56
	v_max_f32_e32 v57, 0, v57
	v_cvt_pk_bf16_f32 v54, v54, v55
	v_cvt_pk_bf16_f32 v55, v56, v57
	ds_write_b64 v64, v[54:55] offset:16384
	v_max_f32_e32 v52, 0, v52
	v_max_f32_e32 v53, 0, v53
	v_cvt_pk_bf16_f32 v50, v50, v51
	v_cvt_pk_bf16_f32 v51, v52, v53
	ds_write_b64 v60, v[50:51] offset:24576
	v_max_f32_e32 v48, 0, v48
	v_max_f32_e32 v49, 0, v49
	v_cvt_pk_bf16_f32 v46, v46, v47
	v_cvt_pk_bf16_f32 v47, v48, v49
	ds_write_b64 v64, v[46:47] offset:32768
	v_max_f32_e32 v44, 0, v44
	v_max_f32_e32 v45, 0, v45
	v_cvt_pk_bf16_f32 v42, v42, v43
	v_cvt_pk_bf16_f32 v43, v44, v45
	ds_write_b64 v60, v[42:43] offset:40960
	v_max_f32_e32 v40, 0, v40
	v_max_f32_e32 v41, 0, v41
	v_cvt_pk_bf16_f32 v38, v38, v39
	v_cvt_pk_bf16_f32 v39, v40, v41
	ds_write_b64 v64, v[38:39] offset:49152
	v_max_f32_e32 v36, 0, v36
	v_max_f32_e32 v37, 0, v37
	v_cvt_pk_bf16_f32 v35, v36, v37
	ds_write_b64 v60, v[34:35] offset:57344
	v_or_b32_e32 v34, 48, v104
	s_waitcnt vmcnt(0)
	v_add_f32_e32 v30, v30, v66
	v_add_f32_e32 v31, v31, v67
	v_add_f32_e32 v32, v32, v68
	v_add_f32_e32 v26, v26, v66
	v_add_f32_e32 v27, v27, v67
	v_add_f32_e32 v28, v28, v68
	v_lshrrev_b32_e32 v34, 3, v34
	v_max_f32_e32 v30, 0, v30
	v_max_f32_e32 v31, 0, v31
	v_max_f32_e32 v32, 0, v32
	v_add_f32_e32 v33, v33, v69
	v_max_f32_e32 v26, 0, v26
	v_max_f32_e32 v27, 0, v27
	v_max_f32_e32 v28, 0, v28
	v_add_f32_e32 v29, v29, v69
	v_max_f32_e32 v33, 0, v33
	v_cvt_pk_bf16_f32 v30, v30, v31
	v_cvt_pk_bf16_f32 v31, v32, v33
	v_xor_b32_e32 v32, v34, v179
	v_max_f32_e32 v29, 0, v29
	v_cvt_pk_bf16_f32 v26, v26, v27
	v_cvt_pk_bf16_f32 v27, v28, v29
	v_bitop3_b32 v28, v34, v179, 16 bitop3:0x1e
	v_add_f32_e32 v2, v2, v66
	v_lshlrev_b32_e32 v32, 4, v32
	v_lshlrev_b32_e32 v28, 4, v28
	v_add_f32_e32 v22, v22, v66
	v_add_f32_e32 v23, v23, v67
	v_add_f32_e32 v18, v18, v66
	v_add_f32_e32 v19, v19, v67
	v_add_f32_e32 v14, v14, v66
	v_add_f32_e32 v15, v15, v67
	v_add_f32_e32 v10, v10, v66
	v_add_f32_e32 v11, v11, v67
	v_add_f32_e32 v6, v6, v66
	v_add_f32_e32 v7, v7, v67
	v_max_f32_e32 v2, 0, v2
	v_add_f32_e32 v3, v3, v67
	v_add3_u32 v32, v103, v32, v102
	v_add3_u32 v28, v103, v28, v102
	v_max_f32_e32 v22, 0, v22
	v_max_f32_e32 v23, 0, v23
	v_add_f32_e32 v24, v24, v68
	v_add_f32_e32 v25, v25, v69
	v_max_f32_e32 v18, 0, v18
	v_max_f32_e32 v19, 0, v19
	v_add_f32_e32 v20, v20, v68
	v_add_f32_e32 v21, v21, v69
	v_max_f32_e32 v14, 0, v14
	v_max_f32_e32 v15, 0, v15
	v_add_f32_e32 v16, v16, v68
	v_add_f32_e32 v17, v17, v69
	v_max_f32_e32 v10, 0, v10
	v_max_f32_e32 v11, 0, v11
	v_add_f32_e32 v12, v12, v68
	v_add_f32_e32 v13, v13, v69
	v_max_f32_e32 v6, 0, v6
	v_max_f32_e32 v7, 0, v7
	v_add_f32_e32 v8, v8, v68
	v_add_f32_e32 v9, v9, v69
	v_max_f32_e32 v3, 0, v3
	v_add_f32_e32 v4, v4, v68
	v_add_f32_e32 v5, v5, v69
	v_cvt_pk_bf16_f32 v2, v2, v3
	ds_write_b64 v32, v[30:31]
	ds_write_b64 v28, v[26:27] offset:8192
	v_max_f32_e32 v24, 0, v24
	v_max_f32_e32 v25, 0, v25
	v_cvt_pk_bf16_f32 v22, v22, v23
	v_cvt_pk_bf16_f32 v23, v24, v25
	ds_write_b64 v32, v[22:23] offset:16384
	v_max_f32_e32 v20, 0, v20
	v_max_f32_e32 v21, 0, v21
	v_cvt_pk_bf16_f32 v18, v18, v19
	v_cvt_pk_bf16_f32 v19, v20, v21
	ds_write_b64 v28, v[18:19] offset:24576
	v_max_f32_e32 v16, 0, v16
	v_max_f32_e32 v17, 0, v17
	v_cvt_pk_bf16_f32 v14, v14, v15
	v_cvt_pk_bf16_f32 v15, v16, v17
	ds_write_b64 v32, v[14:15] offset:32768
	v_max_f32_e32 v12, 0, v12
	v_max_f32_e32 v13, 0, v13
	v_cvt_pk_bf16_f32 v10, v10, v11
	v_cvt_pk_bf16_f32 v11, v12, v13
	ds_write_b64 v28, v[10:11] offset:40960
	v_max_f32_e32 v8, 0, v8
	v_max_f32_e32 v9, 0, v9
	v_cvt_pk_bf16_f32 v6, v6, v7
	v_cvt_pk_bf16_f32 v7, v8, v9
	ds_write_b64 v32, v[6:7] offset:49152
	v_max_f32_e32 v4, 0, v4
	v_max_f32_e32 v5, 0, v5
	v_cvt_pk_bf16_f32 v3, v4, v5
	ds_write_b64 v28, v[2:3] offset:57344
	v_and_b32_e32 v2, 0x1f0, v1
	v_lshrrev_b32_e32 v1, 5, v0
	v_xor_b32_e32 v4, v1, v0
	v_mov_b32_e32 v3, 0
	v_lshlrev_b32_e32 v4, 4, v4
	v_lshl_add_u64 v[12:13], s[4:5], 0, v[2:3]
	v_lshlrev_b32_e32 v2, 9, v1
	v_and_b32_e32 v16, 0x1f0, v4
	v_add3_u32 v2, 0, v2, v16
	s_waitcnt lgkmcnt(0)
	s_barrier
	ds_read_b128 v[4:7], v2
	v_lshlrev_b32_e32 v2, 11, v1
	v_lshl_add_u64 v[14:15], v[12:13], 0, v[2:3]
	v_or_b32_e32 v2, 0x200, v0
	v_lshrrev_b32_e32 v2, 5, v2
	v_xor_b32_e32 v9, v2, v0
	v_lshlrev_b32_e32 v9, 4, v9
	v_lshlrev_b32_e32 v8, 9, v2
	v_and_b32_e32 v9, 0x1f0, v9
	v_add3_u32 v8, 0, v8, v9
	ds_read_b128 v[8:11], v8
	v_lshlrev_b32_e32 v2, 11, v2
	s_waitcnt lgkmcnt(1)
	global_store_dwordx4 v[14:15], v[4:7], off sc1
	s_nop 1
	v_lshl_add_u64 v[4:5], v[12:13], 0, v[2:3]
	s_waitcnt lgkmcnt(0)
	global_store_dwordx4 v[4:5], v[8:11], off sc1
	v_or_b32_e32 v2, 32, v1
	v_lshlrev_b32_e32 v4, 9, v2
	v_or_b32_e32 v8, 0x600, v0
	v_lshrrev_b32_e32 v17, 5, v8
	v_xor_b32_e32 v9, v17, v0
	v_lshlrev_b32_e32 v9, 4, v9
	v_add3_u32 v4, 0, v4, v16
	v_lshlrev_b32_e32 v8, 9, v17
	v_and_b32_e32 v9, 0x1f0, v9
	ds_read_b128 v[4:7], v4
	v_add3_u32 v8, 0, v8, v9
	ds_read_b128 v[8:11], v8
	v_lshlrev_b32_e32 v2, 11, v2
	v_lshl_add_u64 v[14:15], v[12:13], 0, v[2:3]
	v_lshlrev_b32_e32 v2, 11, v17
	s_waitcnt lgkmcnt(1)
	global_store_dwordx4 v[14:15], v[4:7], off sc1
	s_nop 1
	v_lshl_add_u64 v[4:5], v[12:13], 0, v[2:3]
	s_waitcnt lgkmcnt(0)
	global_store_dwordx4 v[4:5], v[8:11], off sc1
	v_or_b32_e32 v2, 64, v1
	v_lshlrev_b32_e32 v4, 9, v2
	v_or_b32_e32 v8, 0xa00, v0
	v_lshrrev_b32_e32 v17, 5, v8
	v_xor_b32_e32 v9, v17, v0
	v_lshlrev_b32_e32 v9, 4, v9
	v_add3_u32 v4, 0, v4, v16
	v_lshlrev_b32_e32 v8, 9, v17
	v_and_b32_e32 v9, 0x1f0, v9
	ds_read_b128 v[4:7], v4
	v_add3_u32 v8, 0, v8, v9
	ds_read_b128 v[8:11], v8
	v_lshlrev_b32_e32 v2, 11, v2
	v_lshl_add_u64 v[14:15], v[12:13], 0, v[2:3]
	v_lshlrev_b32_e32 v2, 11, v17
	s_waitcnt lgkmcnt(1)
	global_store_dwordx4 v[14:15], v[4:7], off sc1
	s_nop 1
	v_lshl_add_u64 v[4:5], v[12:13], 0, v[2:3]
	s_waitcnt lgkmcnt(0)
	global_store_dwordx4 v[4:5], v[8:11], off sc1
	v_or_b32_e32 v2, 0x60, v1
	v_lshlrev_b32_e32 v4, 9, v2
	v_or_b32_e32 v8, 0xe00, v0
	v_lshrrev_b32_e32 v17, 5, v8
	v_xor_b32_e32 v9, v17, v0
	v_lshlrev_b32_e32 v9, 4, v9
	v_add3_u32 v4, 0, v4, v16
	v_lshlrev_b32_e32 v8, 9, v17
	v_and_b32_e32 v9, 0x1f0, v9
	ds_read_b128 v[4:7], v4
	v_add3_u32 v8, 0, v8, v9
	ds_read_b128 v[8:11], v8
	v_lshlrev_b32_e32 v2, 11, v2
	v_lshl_add_u64 v[14:15], v[12:13], 0, v[2:3]
	v_lshlrev_b32_e32 v2, 11, v17
	s_waitcnt lgkmcnt(1)
	global_store_dwordx4 v[14:15], v[4:7], off sc1
	s_nop 1
	v_lshl_add_u64 v[4:5], v[12:13], 0, v[2:3]
	s_waitcnt lgkmcnt(0)
	global_store_dwordx4 v[4:5], v[8:11], off sc1
	v_or_b32_e32 v2, 0x80, v1
	v_lshlrev_b32_e32 v4, 9, v2
	v_or_b32_e32 v8, 0x1200, v0
	v_lshrrev_b32_e32 v17, 5, v8
	v_xor_b32_e32 v9, v17, v0
	v_lshlrev_b32_e32 v9, 4, v9
	v_add3_u32 v4, 0, v4, v16
	v_lshlrev_b32_e32 v8, 9, v17
	v_and_b32_e32 v9, 0x1f0, v9
	ds_read_b128 v[4:7], v4
	v_add3_u32 v8, 0, v8, v9
	ds_read_b128 v[8:11], v8
	v_lshlrev_b32_e32 v2, 11, v2
	v_lshl_add_u64 v[14:15], v[12:13], 0, v[2:3]
	v_lshlrev_b32_e32 v2, 11, v17
	s_waitcnt lgkmcnt(1)
	global_store_dwordx4 v[14:15], v[4:7], off sc1
	s_nop 1
	v_lshl_add_u64 v[4:5], v[12:13], 0, v[2:3]
	s_waitcnt lgkmcnt(0)
	global_store_dwordx4 v[4:5], v[8:11], off sc1
	v_or_b32_e32 v2, 0xa0, v1
	v_lshlrev_b32_e32 v4, 9, v2
	v_or_b32_e32 v8, 0x1600, v0
	v_lshrrev_b32_e32 v17, 5, v8
	v_xor_b32_e32 v9, v17, v0
	v_lshlrev_b32_e32 v9, 4, v9
	v_add3_u32 v4, 0, v4, v16
	v_lshlrev_b32_e32 v8, 9, v17
	v_and_b32_e32 v9, 0x1f0, v9
	ds_read_b128 v[4:7], v4
	v_add3_u32 v8, 0, v8, v9
	ds_read_b128 v[8:11], v8
	v_lshlrev_b32_e32 v2, 11, v2
	v_lshl_add_u64 v[14:15], v[12:13], 0, v[2:3]
	v_lshlrev_b32_e32 v2, 11, v17
	s_waitcnt lgkmcnt(1)
	global_store_dwordx4 v[14:15], v[4:7], off sc1
	s_nop 1
	v_lshl_add_u64 v[4:5], v[12:13], 0, v[2:3]
	s_waitcnt lgkmcnt(0)
	global_store_dwordx4 v[4:5], v[8:11], off sc1
	v_or_b32_e32 v2, 0xc0, v1
	v_lshlrev_b32_e32 v4, 9, v2
	v_or_b32_e32 v8, 0x1a00, v0
	v_lshrrev_b32_e32 v17, 5, v8
	v_xor_b32_e32 v9, v17, v0
	v_add3_u32 v4, 0, v4, v16
	v_lshlrev_b32_e32 v9, 4, v9
	ds_read_b128 v[4:7], v4
	v_lshlrev_b32_e32 v8, 9, v17
	v_and_b32_e32 v9, 0x1f0, v9
	v_add3_u32 v8, 0, v8, v9
	ds_read_b128 v[8:11], v8
	v_lshlrev_b32_e32 v2, 11, v2
	v_lshl_add_u64 v[14:15], v[12:13], 0, v[2:3]
	v_lshlrev_b32_e32 v2, 11, v17
	v_or_b32_e32 v1, 0xe0, v1
	s_waitcnt lgkmcnt(1)
	global_store_dwordx4 v[14:15], v[4:7], off sc1
	s_nop 1
	v_lshl_add_u64 v[4:5], v[12:13], 0, v[2:3]
	v_lshlrev_b32_e32 v2, 9, v1
	v_add3_u32 v2, 0, v2, v16
	s_waitcnt lgkmcnt(0)
	global_store_dwordx4 v[4:5], v[8:11], off sc1
	ds_read_b128 v[4:7], v2
	v_lshlrev_b32_e32 v2, 11, v1
	v_or_b32_e32 v1, 0x1e00, v0
	v_lshrrev_b32_e32 v1, 5, v1
	v_xor_b32_e32 v9, v1, v0
	v_lshlrev_b32_e32 v9, 4, v9
	v_lshlrev_b32_e32 v8, 9, v1
	v_and_b32_e32 v9, 0x1f0, v9
	v_add3_u32 v8, 0, v8, v9
	ds_read_b128 v[8:11], v8
	v_lshl_add_u64 v[14:15], v[12:13], 0, v[2:3]
	v_lshlrev_b32_e32 v2, 11, v1
	s_waitcnt lgkmcnt(1)
	global_store_dwordx4 v[14:15], v[4:7], off sc1
	s_nop 1
	v_lshl_add_u64 v[4:5], v[12:13], 0, v[2:3]
	s_waitcnt lgkmcnt(0)
	global_store_dwordx4 v[4:5], v[8:11], off sc1
	s_waitcnt lgkmcnt(0)
	s_barrier
	s_lshl_b32 s3, s2, 3
	s_and_b32 s3, s3, 56
	s_ashr_i32 s17, s2, 5
	s_add_i32 s20, s3, s17
	s_ashr_i32 s21, s20, 31
	s_bfe_u32 s16, s2, 0x20003
	s_lshl_b64 s[4:5], s[20:21], 17
	s_lshl_b64 s[6:7], s[20:21], 19
	s_add_u32 s6, s12, s6
	s_addc_u32 s7, s13, s7
	s_lshl_b32 s3, s16, 19
	s_add_u32 s3, s14, s3
	v_ashrrev_i32_e32 v2, 6, v0
	v_lshlrev_b32_e32 v1, 4, v0
	s_addc_u32 s13, s15, 0
	v_lshlrev_b32_e32 v4, 9, v2
	v_and_b32_e32 v5, 0x1f0, v1
	s_add_u32 s12, s3, 0x400000
	v_and_or_b32 v32, v4, s0, v5
	v_lshlrev_b32_e32 v4, 5, v2
	v_and_b32_e32 v5, 48, v1
	s_addc_u32 s13, s13, 0
	v_bitop3_b32 v4, v4, v5, 32 bitop3:0x6c
	s_and_b32 s15, s2, 8
	s_add_i32 s3, s20, 3
	v_bfe_u32 v31, v0, 5, 1
	v_lshrrev_b32_e32 v34, 1, v4
	v_add_u32_e32 v4, s15, v2
	s_mov_b32 s20, 0x3ffffe
	v_and_or_b32 v30, v4, s20, v31
	v_bfe_i32 v5, v30, 0, 22
	v_bfe_u32 v4, v30, 21, 1
	v_add_u32_e32 v6, v5, v4
	v_lshlrev_b32_e32 v4, 3, v6
	v_and_b32_e32 v6, 0x7fffffe, v6
	s_lshl_b32 s0, s17, 4
	v_sub_u32_e32 v5, v5, v6
	s_and_b32 s17, s0, 16
	v_lshl_or_b32 v6, v5, 5, v34
	v_add_u32_e32 v5, s17, v2
	v_and_or_b32 v35, v5, s20, v31
	v_bfe_i32 v7, v35, 0, 22
	v_bfe_u32 v8, v35, 21, 1
	v_add_u32_e32 v8, v7, v8
	v_lshlrev_b32_e32 v9, 3, v8
	v_and_b32_e32 v8, 0x7fffffe, v8
	v_add_u32_e32 v5, 8, v5
	v_sub_u32_e32 v7, v7, v8
	v_and_or_b32 v36, v5, s20, v31
	v_lshl_or_b32 v98, v7, 5, v34
	v_bfe_i32 v5, v36, 0, 22
	v_bfe_u32 v7, v36, 21, 1
	v_add_u32_e32 v7, v5, v7
	v_lshrrev_b32_e32 v33, 6, v32
	v_lshlrev_b32_e32 v8, 3, v7
	v_and_b32_e32 v7, 0x7fffffe, v7
	s_and_b32 s3, s3, 15
	v_and_or_b32 v4, v4, -16, v33
	v_sub_u32_e32 v5, v5, v7
	v_and_or_b32 v14, v9, -16, v33
	v_lshl_or_b32 v100, v5, 5, v34
	v_ashrrev_i32_e32 v5, 31, v4
	s_lshl_b32 s14, s3, 6
	s_lshl_b32 s0, s3, 8
	s_lshl_b32 s2, s3, 7
	v_and_or_b32 v16, v8, -16, v33
	v_lshlrev_b64 v[4:5], 12, v[4:5]
	s_add_u32 s2, s12, s2
	v_ashrrev_i32_e32 v15, 31, v14
	v_lshl_add_u64 v[4:5], s[6:7], 0, v[4:5]
	v_ashrrev_i32_e32 v7, 31, v6
	s_addc_u32 s3, s13, 0
	v_lshlrev_b64 v[102:103], 11, v[14:15]
	v_ashrrev_i32_e32 v99, 31, v98
	v_ashrrev_i32_e32 v17, 31, v16
	v_lshl_add_u64 v[8:9], v[4:5], 0, s[0:1]
	v_lshlrev_b64 v[38:39], 2, v[6:7]
	v_lshl_add_u64 v[14:15], s[2:3], 0, v[102:103]
	v_lshlrev_b64 v[22:23], 1, v[98:99]
	v_lshlrev_b64 v[104:105], 11, v[16:17]
	v_ashrrev_i32_e32 v101, 31, v100
	v_lshl_add_u64 v[18:19], v[8:9], 0, v[38:39]
	v_lshl_add_u64 v[24:25], v[14:15], 0, v[22:23]
	v_lshl_add_u64 v[14:15], s[2:3], 0, v[104:105]
	v_lshlrev_b64 v[26:27], 1, v[100:101]
	global_load_dwordx4 v[6:9], v[18:19], off offset:16
	global_load_dwordx4 v[10:13], v[18:19], off
	v_lshl_add_u64 v[28:29], v[14:15], 0, v[26:27]
	global_load_dwordx4 v[14:17], v[24:25], off
	global_load_dwordx4 v[18:21], v[28:29], off
	v_lshlrev_b32_e32 v24, 10, v30
	v_or_b32_e32 v125, v24, v32
	v_xad_u32 v24, s15, 8, v2
	v_and_or_b32 v24, v24, s20, v31
	v_lshlrev_b32_e32 v25, 10, v24
	v_or_b32_e32 v122, v25, v32
	v_bfe_i32 v25, v24, 0, 22
	v_bfe_u32 v24, v24, 21, 1
	v_add_u32_e32 v28, v25, v24
	v_lshlrev_b32_e32 v24, 3, v28
	v_and_b32_e32 v28, 0x7fffffe, v28
	v_sub_u32_e32 v25, v25, v28
	v_lshl_or_b32 v28, v25, 5, v34
	v_lshlrev_b32_e32 v25, 10, v35
	v_or_b32_e32 v126, v25, v32
	v_lshlrev_b32_e32 v25, 10, v36
	v_or_b32_e32 v127, v25, v32
	v_xad_u32 v25, s17, 16, v2
	v_and_or_b32 v25, v25, s20, v31
	v_lshlrev_b32_e32 v29, 10, v25
	v_or_b32_e32 v123, v29, v32
	v_bfe_i32 v29, v25, 0, 22
	v_bfe_u32 v25, v25, 21, 1
	v_add_u32_e32 v25, v29, v25
	v_and_b32_e32 v121, 3, v2
	v_lshlrev_b32_e32 v30, 3, v25
	v_and_b32_e32 v25, 0x7fffffe, v25
	v_xad_u32 v2, s17, 24, v2
	v_sub_u32_e32 v25, v29, v25
	v_and_or_b32 v2, v2, s20, v31
	v_lshl_or_b32 v106, v25, 5, v34
	v_lshlrev_b32_e32 v25, 10, v2
	v_or_b32_e32 v124, v25, v32
	v_bfe_i32 v25, v2, 0, 22
	v_bfe_u32 v2, v2, 21, 1
	v_add_u32_e32 v2, v25, v2
	v_lshlrev_b32_e32 v29, 3, v2
	v_and_b32_e32 v2, 0x7fffffe, v2
	v_and_b32_e32 v118, 15, v0
	v_sub_u32_e32 v2, v25, v2
	v_lshlrev_b32_e32 v25, 2, v0
	v_ashrrev_i32_e32 v120, 8, v0
	v_and_or_b32 v32, v29, -16, v33
	v_lshl_or_b32 v108, v2, 5, v34
	v_and_b32_e32 v2, 48, v0
	v_and_b32_e32 v25, 32, v25
	v_lshlrev_b32_e32 v29, 6, v118
	v_and_b32_e32 v119, 63, v0
	v_and_or_b32 v24, v24, -16, v33
	v_and_or_b32 v30, v30, -16, v33
	v_lshlrev_b32_e32 v68, 13, v120
	v_bitop3_b32 v2, v29, v25, v2 bitop3:0x36
	v_ashrrev_i32_e32 v25, 31, v24
	v_lshlrev_b64 v[24:25], 12, v[24:25]
	v_lshl_add_u64 v[56:57], s[6:7], 0, v[24:25]
	v_ashrrev_i32_e32 v29, 31, v28
	v_lshl_add_u64 v[24:25], v[56:57], 0, s[0:1]
	v_lshlrev_b64 v[58:59], 2, v[28:29]
	v_ashrrev_i32_e32 v31, 31, v30
	v_lshl_add_u64 v[24:25], v[24:25], 0, v[58:59]
	v_lshlrev_b64 v[110:111], 11, v[30:31]
	v_ashrrev_i32_e32 v107, 31, v106
	v_ashrrev_i32_e32 v33, 31, v32
	global_load_dwordx4 v[40:43], v[24:25], off offset:16
	global_load_dwordx4 v[44:47], v[24:25], off
	v_lshl_add_u64 v[24:25], s[2:3], 0, v[110:111]
	v_lshlrev_b64 v[60:61], 1, v[106:107]
	v_lshlrev_b64 v[112:113], 11, v[32:33]
	v_ashrrev_i32_e32 v109, 31, v108
	v_lshl_add_u64 v[24:25], v[24:25], 0, v[60:61]
	v_lshl_add_u64 v[28:29], s[2:3], 0, v[112:113]
	v_lshlrev_b64 v[62:63], 1, v[108:109]
	v_lshl_add_u64 v[28:29], v[28:29], 0, v[62:63]
	global_load_dwordx4 v[48:51], v[24:25], off
	global_load_dwordx4 v[52:55], v[28:29], off
	s_add_i32 s0, s14, 64
	s_and_b32 s2, s0, 0x3c0
	s_lshl_b32 s0, s2, 2
	s_lshl_b32 s2, s2, 1
	v_lshl_add_u64 v[24:25], v[4:5], 0, s[0:1]
	s_add_u32 s2, s12, s2
	v_lshl_add_u64 v[24:25], v[24:25], 0, v[38:39]
	s_addc_u32 s3, s13, 0
	global_load_dwordx4 v[30:33], v[24:25], off offset:16
	global_load_dwordx4 v[34:37], v[24:25], off
	v_lshl_add_u64 v[24:25], s[2:3], 0, v[102:103]
	v_lshl_add_u64 v[64:65], v[24:25], 0, v[22:23]
	v_lshl_add_u64 v[22:23], s[2:3], 0, v[104:105]
	v_lshl_add_u64 v[66:67], v[22:23], 0, v[26:27]
	global_load_dwordx4 v[26:29], v[64:65], off
	global_load_dwordx4 v[22:25], v[66:67], off
	v_add_u32_e32 v64, 0, v125
	s_waitcnt vmcnt(10)
	v_cvt_pk_bf16_f32 v10, v10, v11
	v_cvt_pk_bf16_f32 v11, v12, v13
	v_cvt_pk_bf16_f32 v12, v6, v7
	v_add_u32_e32 v6, 0, v126
	v_cvt_pk_bf16_f32 v13, v8, v9
	ds_write_b128 v64, v[10:13]
	s_waitcnt vmcnt(9)
	ds_write_b128 v6, v[14:17] offset:32768
	v_add_u32_e32 v6, 0, v127
	s_waitcnt vmcnt(8)
	ds_write_b128 v6, v[18:21] offset:32768
	v_add_u32_e32 v10, 0, v122
	s_waitcnt vmcnt(6)
	v_cvt_pk_bf16_f32 v6, v44, v45
	v_cvt_pk_bf16_f32 v7, v46, v47
	v_cvt_pk_bf16_f32 v8, v40, v41
	v_cvt_pk_bf16_f32 v9, v42, v43
	ds_write_b128 v10, v[6:9]
	v_add_u32_e32 v6, 0, v123
	s_waitcnt vmcnt(5)
	ds_write_b128 v6, v[48:51] offset:32768
	v_add_u32_e32 v6, 0, v124
	s_waitcnt vmcnt(4)
	ds_write_b128 v6, v[52:55] offset:32768
	v_lshl_add_u64 v[6:7], v[56:57], 0, s[0:1]
	v_lshl_add_u64 v[14:15], v[6:7], 0, v[58:59]
	global_load_dwordx4 v[6:9], v[14:15], off offset:16
	global_load_dwordx4 v[10:13], v[14:15], off
	v_lshl_add_u64 v[14:15], s[2:3], 0, v[110:111]
	v_lshl_add_u64 v[40:41], v[14:15], 0, v[60:61]
	v_lshl_add_u64 v[14:15], s[2:3], 0, v[112:113]
	v_lshl_add_u64 v[42:43], v[14:15], 0, v[62:63]
	global_load_dwordx4 v[18:21], v[40:41], off
	global_load_dwordx4 v[14:17], v[42:43], off
	v_lshlrev_b32_e32 v40, 13, v121
	s_cmp_lg_u32 0, -1
	s_waitcnt lgkmcnt(0)
	s_cselect_b32 s0, 0, 0
	v_add3_u32 v128, v68, s0, v2
	s_add_i32 s0, s0, 0x8000
	v_add3_u32 v129, v40, s0, v2
	v_lshl_add_u64 v[114:115], v[4:5], 0, v[38:39]
	v_lshl_add_u64 v[116:117], v[56:57], 0, v[58:59]
	s_add_i32 s2, s14, 0x80
	s_mov_b32 s3, 0
	v_mov_b32_e32 v2, v3
	v_mov_b32_e32 v4, v3
	v_mov_b32_e32 v5, v3
	v_mov_b32_e32 v38, v3
	v_mov_b32_e32 v39, v3
	v_mov_b32_e32 v40, v3
	v_mov_b32_e32 v41, v3
	v_mov_b32_e32 v42, v3
	v_mov_b32_e32 v43, v3
	v_mov_b32_e32 v44, v3
	v_mov_b32_e32 v45, v3
	v_mov_b32_e32 v46, v3
	v_mov_b32_e32 v47, v3
	v_mov_b32_e32 v48, v3
	v_mov_b32_e32 v49, v3
	v_mov_b32_e32 v50, v3
	v_mov_b32_e32 v51, v3
	v_mov_b32_e32 v52, v3
	v_mov_b32_e32 v53, v3
	v_mov_b32_e32 v54, v3
	v_mov_b32_e32 v55, v3
	v_mov_b32_e32 v56, v3
	v_mov_b32_e32 v57, v3
	v_mov_b32_e32 v58, v3
	v_mov_b32_e32 v59, v3
	v_mov_b32_e32 v60, v3
	v_mov_b32_e32 v61, v3
	v_mov_b32_e32 v62, v3
	v_mov_b32_e32 v63, v3
	v_mov_b32_e32 v64, v3
	v_mov_b32_e32 v65, v3
	v_mov_b32_e32 v66, v3
	v_mov_b32_e32 v67, v3
	v_mov_b32_e32 v68, v3
	v_mov_b32_e32 v69, v3
	v_mov_b32_e32 v70, v3
	v_mov_b32_e32 v71, v3
	v_mov_b32_e32 v72, v3
	v_mov_b32_e32 v73, v3
	v_mov_b32_e32 v74, v3
	v_mov_b32_e32 v75, v3
	v_mov_b32_e32 v76, v3
	v_mov_b32_e32 v77, v3
	v_mov_b32_e32 v78, v3
	v_mov_b32_e32 v79, v3
	v_mov_b32_e32 v80, v3
	v_mov_b32_e32 v81, v3
	v_mov_b32_e32 v82, v3
	v_mov_b32_e32 v83, v3
	v_mov_b32_e32 v84, v3
	v_mov_b32_e32 v85, v3
	v_mov_b32_e32 v86, v3
	v_mov_b32_e32 v87, v3
	v_mov_b32_e32 v88, v3
	v_mov_b32_e32 v89, v3
	v_mov_b32_e32 v90, v3
	v_mov_b32_e32 v91, v3
	v_mov_b32_e32 v92, v3
	v_mov_b32_e32 v93, v3
	v_mov_b32_e32 v94, v3
	v_mov_b32_e32 v95, v3
	v_mov_b32_e32 v96, v3
	v_mov_b32_e32 v97, v3
	s_barrier
	s_cmp_lg_u32 s40, 0
	s_cbranch_scc1 .Lrot2_loop

.Lrot2_done:
	ds_read_b128 v[98:101], v129 offset:0
	ds_read_b128 v[102:105], v129 offset:0x800
	ds_read_b128 v[106:109], v129 offset:0x1000
	ds_read_b128 v[110:113], v129 offset:0x1800
	ds_read_b128 v[114:117], v128 offset:0
	ds_read_b128 v[130:133], v128 offset:0x800
	ds_read_b128 v[134:137], v128 offset:0x1000
	s_waitcnt lgkmcnt(2)
	v_mfma_f32_16x16x32_bf16 v[94:97], v[98:101], v[114:117], v[94:97]
	v_mfma_f32_16x16x32_bf16 v[90:93], v[102:105], v[114:117], v[90:93]
	v_mfma_f32_16x16x32_bf16 v[86:89], v[106:109], v[114:117], v[86:89]
	v_mfma_f32_16x16x32_bf16 v[82:85], v[110:113], v[114:117], v[82:85]
	ds_read_b128 v[114:117], v128 offset:0x1800
	s_waitcnt lgkmcnt(2)
	v_mfma_f32_16x16x32_bf16 v[78:81], v[98:101], v[130:133], v[78:81]
	v_mfma_f32_16x16x32_bf16 v[74:77], v[102:105], v[130:133], v[74:77]
	v_mfma_f32_16x16x32_bf16 v[70:73], v[106:109], v[130:133], v[70:73]
	v_mfma_f32_16x16x32_bf16 v[66:69], v[110:113], v[130:133], v[66:69]
	s_waitcnt lgkmcnt(1)
	v_mfma_f32_16x16x32_bf16 v[62:65], v[98:101], v[134:137], v[62:65]
	v_mfma_f32_16x16x32_bf16 v[58:61], v[102:105], v[134:137], v[58:61]
	v_mfma_f32_16x16x32_bf16 v[54:57], v[106:109], v[134:137], v[54:57]
	v_mfma_f32_16x16x32_bf16 v[50:53], v[110:113], v[134:137], v[50:53]
	s_waitcnt lgkmcnt(0)
	v_mfma_f32_16x16x32_bf16 v[46:49], v[98:101], v[114:117], v[46:49]
	v_mfma_f32_16x16x32_bf16 v[42:45], v[102:105], v[114:117], v[42:45]
	v_mfma_f32_16x16x32_bf16 v[38:41], v[106:109], v[114:117], v[38:41]
	v_mfma_f32_16x16x32_bf16 v[2:5], v[110:113], v[114:117], v[2:5]
	v_add_u32_e32 v98, s18, v125
	s_waitcnt vmcnt(6)
	v_cvt_pk_bf16_f32 v34, v34, v35
	v_cvt_pk_bf16_f32 v35, v36, v37
	v_cvt_pk_bf16_f32 v36, v30, v31
	v_add_u32_e32 v30, s19, v126
	v_cvt_pk_bf16_f32 v37, v32, v33
	ds_write_b128 v98, v[34:37]
	s_waitcnt vmcnt(5)
	ds_write_b128 v30, v[26:29]
	v_add_u32_e32 v26, s19, v127
	s_waitcnt vmcnt(4)
	ds_write_b128 v26, v[22:25]
	ds_read_b128 v[22:25], v129 offset:0x400
	ds_read_b128 v[26:29], v129 offset:0xc00
	ds_read_b128 v[30:33], v129 offset:0x1400
	ds_read_b128 v[34:37], v129 offset:0x1c00
	ds_read_b128 v[98:101], v128 offset:0x400
	ds_read_b128 v[102:105], v128 offset:0xc00
	ds_read_b128 v[106:109], v128 offset:0x1400
	s_waitcnt lgkmcnt(2)
	v_mfma_f32_16x16x32_bf16 v[94:97], v[22:25], v[98:101], v[94:97]
	v_mfma_f32_16x16x32_bf16 v[90:93], v[26:29], v[98:101], v[90:93]
	v_mfma_f32_16x16x32_bf16 v[86:89], v[30:33], v[98:101], v[86:89]
	v_mfma_f32_16x16x32_bf16 v[82:85], v[34:37], v[98:101], v[82:85]
	ds_read_b128 v[98:101], v128 offset:0x1c00
	s_waitcnt lgkmcnt(2)
	v_mfma_f32_16x16x32_bf16 v[78:81], v[22:25], v[102:105], v[78:81]
	v_mfma_f32_16x16x32_bf16 v[74:77], v[26:29], v[102:105], v[74:77]
	v_mfma_f32_16x16x32_bf16 v[70:73], v[30:33], v[102:105], v[70:73]
	v_mfma_f32_16x16x32_bf16 v[66:69], v[34:37], v[102:105], v[66:69]
	s_waitcnt lgkmcnt(1)
	v_mfma_f32_16x16x32_bf16 v[62:65], v[22:25], v[106:109], v[62:65]
	v_mfma_f32_16x16x32_bf16 v[58:61], v[26:29], v[106:109], v[58:61]
	v_mfma_f32_16x16x32_bf16 v[54:57], v[30:33], v[106:109], v[54:57]
	v_mfma_f32_16x16x32_bf16 v[50:53], v[34:37], v[106:109], v[50:53]
	s_waitcnt lgkmcnt(0)
	v_mfma_f32_16x16x32_bf16 v[22:25], v[22:25], v[98:101], v[46:49]
	v_mfma_f32_16x16x32_bf16 v[26:29], v[26:29], v[98:101], v[42:45]
	v_mfma_f32_16x16x32_bf16 v[30:33], v[30:33], v[98:101], v[38:41]
	v_mfma_f32_16x16x32_bf16 v[2:5], v[34:37], v[98:101], v[2:5]
	v_add_u32_e32 v34, s18, v122
	s_waitcnt vmcnt(2)
	v_cvt_pk_bf16_f32 v10, v10, v11
	v_cvt_pk_bf16_f32 v11, v12, v13
	v_cvt_pk_bf16_f32 v12, v6, v7
	v_add_u32_e32 v6, s19, v123
	s_lshl_b64 s[0:1], s[4:5], 1
	v_cvt_pk_bf16_f32 v13, v8, v9
	ds_write_b128 v34, v[10:13]
	s_waitcnt vmcnt(1)
	ds_write_b128 v6, v[18:21]
	v_add_u32_e32 v6, s19, v124
	s_add_u32 s0, s10, s0
	s_waitcnt vmcnt(0)
	ds_write_b128 v6, v[14:17]
	s_addc_u32 s1, s11, s1
	s_lshl_b32 s2, s16, 9
	s_waitcnt lgkmcnt(0)
	s_barrier
	v_add_u32_e32 v110, 0x10000, v128
	v_add_u32_e32 v102, 0x10000, v129
	ds_read_b128 v[6:9], v102 offset:0
	ds_read_b128 v[10:13], v102 offset:0x800
	ds_read_b128 v[14:17], v102 offset:0x1000
	ds_read_b128 v[18:21], v102 offset:0x1800
	ds_read_b128 v[34:37], v110 offset:0
	ds_read_b128 v[38:41], v110 offset:0x800
	ds_read_b128 v[42:45], v110 offset:0x1000
	s_add_u32 s0, s0, s2
	s_addc_u32 s1, s1, 0
	s_lshl_b32 s2, s16, 10
	s_waitcnt lgkmcnt(2)
	s_add_u32 s2, s8, s2
	v_mfma_f32_16x16x32_bf16 v[46:49], v[6:9], v[34:37], v[94:97]
	s_addc_u32 s3, s9, 0
	v_mfma_f32_16x16x32_bf16 v[90:93], v[10:13], v[34:37], v[90:93]
	v_mfma_f32_16x16x32_bf16 v[86:89], v[14:17], v[34:37], v[86:89]
	v_mfma_f32_16x16x32_bf16 v[34:37], v[18:21], v[34:37], v[82:85]
	ds_read_b128 v[82:85], v110 offset:0x1800
	s_waitcnt lgkmcnt(2)
	v_mfma_f32_16x16x32_bf16 v[78:81], v[6:9], v[38:41], v[78:81]
	v_mfma_f32_16x16x32_bf16 v[74:77], v[10:13], v[38:41], v[74:77]
	v_mfma_f32_16x16x32_bf16 v[70:73], v[14:17], v[38:41], v[70:73]
	v_mfma_f32_16x16x32_bf16 v[38:41], v[18:21], v[38:41], v[66:69]
	s_waitcnt lgkmcnt(1)
	v_mfma_f32_16x16x32_bf16 v[62:65], v[6:9], v[42:45], v[62:65]
	v_mfma_f32_16x16x32_bf16 v[58:61], v[10:13], v[42:45], v[58:61]
	v_mfma_f32_16x16x32_bf16 v[54:57], v[14:17], v[42:45], v[54:57]
	v_mfma_f32_16x16x32_bf16 v[42:45], v[18:21], v[42:45], v[50:53]
	s_waitcnt lgkmcnt(0)
	v_mfma_f32_16x16x32_bf16 v[50:53], v[6:9], v[82:85], v[22:25]
	v_mfma_f32_16x16x32_bf16 v[66:69], v[10:13], v[82:85], v[26:29]
	v_mfma_f32_16x16x32_bf16 v[94:97], v[14:17], v[82:85], v[30:33]
	v_mfma_f32_16x16x32_bf16 v[2:5], v[18:21], v[82:85], v[2:5]
	ds_read_b128 v[18:21], v102 offset:0x400
	ds_read_b128 v[82:85], v102 offset:0xc00
	ds_read_b128 v[98:101], v102 offset:0x1400
	ds_read_b128 v[102:105], v102 offset:0x1c00
	ds_read_b128 v[6:9], v110 offset:0x400
	ds_read_b128 v[10:13], v110 offset:0xc00
	ds_read_b128 v[106:109], v110 offset:0x1400
	s_waitcnt lgkmcnt(2)
	v_mfma_f32_16x16x32_bf16 v[46:49], v[18:21], v[6:9], v[46:49]
	v_mfma_f32_16x16x32_bf16 v[90:93], v[82:85], v[6:9], v[90:93]
	v_mfma_f32_16x16x32_bf16 v[30:33], v[98:101], v[6:9], v[86:89]
	v_mfma_f32_16x16x32_bf16 v[14:17], v[102:105], v[6:9], v[34:37]
	ds_read_b128 v[86:89], v110 offset:0x1c00
	s_waitcnt lgkmcnt(2)
	v_mfma_f32_16x16x32_bf16 v[78:81], v[18:21], v[10:13], v[78:81]
	v_mfma_f32_16x16x32_bf16 v[74:77], v[82:85], v[10:13], v[74:77]
	v_mfma_f32_16x16x32_bf16 v[26:29], v[98:101], v[10:13], v[70:73]
	v_mfma_f32_16x16x32_bf16 v[10:13], v[102:105], v[10:13], v[38:41]
	s_waitcnt lgkmcnt(1)
	v_mfma_f32_16x16x32_bf16 v[62:65], v[18:21], v[106:109], v[62:65]
	v_mfma_f32_16x16x32_bf16 v[38:41], v[82:85], v[106:109], v[58:61]
	v_mfma_f32_16x16x32_bf16 v[22:25], v[98:101], v[106:109], v[54:57]
	v_mfma_f32_16x16x32_bf16 v[6:9], v[102:105], v[106:109], v[42:45]
	s_waitcnt lgkmcnt(0)
	v_mfma_f32_16x16x32_bf16 v[42:45], v[18:21], v[86:89], v[50:53]
	v_mfma_f32_16x16x32_bf16 v[34:37], v[82:85], v[86:89], v[66:69]
	v_mfma_f32_16x16x32_bf16 v[18:21], v[98:101], v[86:89], v[94:97]
	v_mfma_f32_16x16x32_bf16 v[2:5], v[102:105], v[86:89], v[2:5]
	v_lshrrev_b32_e32 v50, 2, v119
	v_and_b32_e32 v50, 12, v50
	v_lshl_or_b32 v66, v121, 6, v50
	v_lshlrev_b32_e32 v67, 2, v66
	s_waitcnt lgkmcnt(0)
	s_barrier
	global_load_dwordx4 v[50:53], v67, s[2:3]
	global_load_dwordx4 v[54:57], v67, s[2:3] offset:64
	v_lshrrev_b32_e32 v58, 1, v119
	v_lshl_or_b32 v59, v120, 6, v118
	v_and_b32_e32 v68, 8, v58
	v_lshl_add_u32 v69, v59, 9, 0
	v_or_b32_e32 v70, 16, v59
	v_or_b32_e32 v71, 48, v59
	v_lshrrev_b32_e32 v58, 3, v66
	v_or_b32_e32 v59, 16, v66
	v_bitop3_b32 v83, v70, v58, 31 bitop3:0x6c
	v_lshrrev_b32_e32 v85, 3, v59
	v_lshl_add_u32 v72, v70, 9, 0
	v_xor_b32_e32 v82, v58, v118
	v_bitop3_b32 v84, v71, v58, 31 bitop3:0x6c
	v_lshlrev_b32_e32 v83, 4, v83
	v_xor_b32_e32 v86, v85, v118
	v_lshl_add_u32 v73, v71, 9, 0
	v_lshlrev_b32_e32 v82, 4, v82
	v_lshlrev_b32_e32 v84, 4, v84
	v_add3_u32 v83, v72, v83, v68
	v_lshlrev_b32_e32 v86, 4, v86
	global_load_dwordx4 v[58:61], v67, s[2:3] offset:128
	v_add3_u32 v82, v69, v82, v68
	v_add3_u32 v84, v73, v84, v68
	v_add3_u32 v86, v69, v86, v68
	s_waitcnt vmcnt(2)
	v_add_f32_e32 v46, v46, v50
	v_add_f32_e32 v47, v47, v51
	v_add_f32_e32 v48, v48, v52
	v_add_f32_e32 v49, v49, v53
	v_add_f32_e32 v78, v78, v50
	v_add_f32_e32 v79, v79, v51
	v_add_f32_e32 v80, v80, v52
	v_add_f32_e32 v81, v81, v53
	v_add_f32_e32 v62, v62, v50
	v_add_f32_e32 v63, v63, v51
	v_add_f32_e32 v42, v42, v50
	v_add_f32_e32 v43, v43, v51
	v_add_f32_e32 v44, v44, v52
	v_add_f32_e32 v45, v45, v53
	s_waitcnt vmcnt(1)
	v_add_f32_e32 v50, v90, v54
	v_add_f32_e32 v51, v91, v55
	v_add_f32_e32 v64, v64, v52
	v_add_f32_e32 v65, v65, v53
	v_add_f32_e32 v52, v92, v56
	v_add_f32_e32 v53, v93, v57
	v_max_f32_e32 v46, 0, v46
	v_max_f32_e32 v47, 0, v47
	v_max_f32_e32 v48, 0, v48
	v_max_f32_e32 v49, 0, v49
	v_max_f32_e32 v78, 0, v78
	v_max_f32_e32 v79, 0, v79
	v_max_f32_e32 v80, 0, v80
	v_max_f32_e32 v81, 0, v81
	v_max_f32_e32 v88, 0, v43
	v_max_f32_e32 v89, 0, v44
	v_max_f32_e32 v90, 0, v45
	v_max_f32_e32 v50, 0, v50
	v_max_f32_e32 v51, 0, v51
	v_cvt_pk_bf16_f32 v43, v48, v49
	v_cvt_pk_bf16_f32 v44, v78, v79
	v_cvt_pk_bf16_f32 v45, v80, v81
	v_max_f32_e32 v62, 0, v62
	v_max_f32_e32 v63, 0, v63
	v_max_f32_e32 v64, 0, v64
	v_max_f32_e32 v65, 0, v65
	v_max_f32_e32 v87, 0, v42
	v_max_f32_e32 v52, 0, v52
	v_max_f32_e32 v53, 0, v53
	v_cvt_pk_bf16_f32 v42, v46, v47
	v_cvt_pk_bf16_f32 v46, v62, v63
	v_cvt_pk_bf16_f32 v47, v64, v65
	v_cvt_pk_bf16_f32 v48, v87, v88
	v_cvt_pk_bf16_f32 v49, v89, v90
	v_cvt_pk_bf16_f32 v50, v50, v51
	v_cvt_pk_bf16_f32 v51, v52, v53
	ds_write_b64 v83, v[44:45]
	ds_write2st64_b64 v82, v[42:43], v[46:47] offset1:32
	ds_write_b64 v84, v[48:49]
	ds_write_b64 v86, v[50:51]
	v_add_f32_e32 v43, v76, v56
	v_add_f32_e32 v44, v77, v57
	v_max_f32_e32 v43, 0, v43
	v_max_f32_e32 v44, 0, v44
	v_add_f32_e32 v42, v75, v55
	v_cvt_pk_bf16_f32 v43, v43, v44
	v_bitop3_b32 v44, v85, v70, 31 bitop3:0x78
	v_add_f32_e32 v74, v74, v54
	v_max_f32_e32 v42, 0, v42
	v_lshlrev_b32_e32 v44, 4, v44
	v_max_f32_e32 v74, 0, v74
	v_cvt_pk_bf16_f32 v42, v74, v42
	v_add3_u32 v44, v72, v44, v68
	ds_write_b64 v44, v[42:43]
	global_load_dwordx4 v[42:45], v67, s[2:3] offset:192
	v_add_f32_e32 v34, v34, v54
	v_add_f32_e32 v35, v35, v55
	v_add_f32_e32 v36, v36, v56
	v_max_f32_e32 v34, 0, v34
	v_max_f32_e32 v35, 0, v35
	v_max_f32_e32 v36, 0, v36
	v_add_f32_e32 v37, v37, v57
	v_max_f32_e32 v37, 0, v37
	v_cvt_pk_bf16_f32 v34, v34, v35
	v_cvt_pk_bf16_f32 v35, v36, v37
	v_bitop3_b32 v36, v85, v71, 31 bitop3:0x78
	v_add_f32_e32 v38, v38, v54
	v_add_f32_e32 v39, v39, v55
	v_lshlrev_b32_e32 v36, 4, v36
	v_max_f32_e32 v38, 0, v38
	v_max_f32_e32 v39, 0, v39
	v_add_f32_e32 v40, v40, v56
	v_add_f32_e32 v41, v41, v57
	v_add3_u32 v36, v73, v36, v68
	v_max_f32_e32 v40, 0, v40
	v_max_f32_e32 v41, 0, v41
	v_cvt_pk_bf16_f32 v38, v38, v39
	v_cvt_pk_bf16_f32 v39, v40, v41
	ds_write_b64 v86, v[38:39] offset:16384
	ds_write_b64 v36, v[34:35]
	v_or_b32_e32 v34, 32, v66
	s_waitcnt vmcnt(1)
	v_add_f32_e32 v30, v30, v58
	v_add_f32_e32 v31, v31, v59
	v_add_f32_e32 v32, v32, v60
	v_add_f32_e32 v26, v26, v58
	v_add_f32_e32 v27, v27, v59
	v_add_f32_e32 v28, v28, v60
	v_add_f32_e32 v18, v18, v58
	v_add_f32_e32 v19, v19, v59
	v_add_f32_e32 v20, v20, v60
	v_lshrrev_b32_e32 v34, 3, v34
	v_max_f32_e32 v30, 0, v30
	v_max_f32_e32 v31, 0, v31
	v_max_f32_e32 v32, 0, v32
	v_add_f32_e32 v33, v33, v61
	v_max_f32_e32 v26, 0, v26
	v_max_f32_e32 v27, 0, v27
	v_max_f32_e32 v28, 0, v28
	v_add_f32_e32 v29, v29, v61
	v_max_f32_e32 v18, 0, v18
	v_max_f32_e32 v19, 0, v19
	v_max_f32_e32 v20, 0, v20
	v_add_f32_e32 v21, v21, v61
	v_max_f32_e32 v33, 0, v33
	v_cvt_pk_bf16_f32 v30, v30, v31
	v_cvt_pk_bf16_f32 v31, v32, v33
	v_xor_b32_e32 v32, v34, v118
	v_max_f32_e32 v29, 0, v29
	v_cvt_pk_bf16_f32 v26, v26, v27
	v_cvt_pk_bf16_f32 v27, v28, v29
	v_bitop3_b32 v28, v34, v70, 31 bitop3:0x78
	v_max_f32_e32 v21, 0, v21
	v_cvt_pk_bf16_f32 v18, v18, v19
	v_cvt_pk_bf16_f32 v19, v20, v21
	v_bitop3_b32 v20, v34, v71, 31 bitop3:0x78
	v_lshlrev_b32_e32 v32, 4, v32
	v_lshlrev_b32_e32 v28, 4, v28
	v_add_f32_e32 v22, v22, v58
	v_add_f32_e32 v23, v23, v59
	v_lshlrev_b32_e32 v20, 4, v20
	v_add3_u32 v32, v69, v32, v68
	v_add3_u32 v28, v72, v28, v68
	v_max_f32_e32 v22, 0, v22
	v_max_f32_e32 v23, 0, v23
	v_add_f32_e32 v24, v24, v60
	v_add_f32_e32 v25, v25, v61
	v_add3_u32 v20, v73, v20, v68
	ds_write_b64 v32, v[30:31]
	ds_write_b64 v28, v[26:27]
	v_max_f32_e32 v24, 0, v24
	v_max_f32_e32 v25, 0, v25
	v_cvt_pk_bf16_f32 v22, v22, v23
	v_cvt_pk_bf16_f32 v23, v24, v25
	ds_write_b64 v32, v[22:23] offset:16384
	ds_write_b64 v20, v[18:19]
	v_or_b32_e32 v18, 48, v66
	s_waitcnt vmcnt(0)
	v_add_f32_e32 v14, v14, v42
	v_add_f32_e32 v15, v15, v43
	v_add_f32_e32 v16, v16, v44
	v_add_f32_e32 v10, v10, v42
	v_add_f32_e32 v11, v11, v43
	v_add_f32_e32 v12, v12, v44
	v_add_f32_e32 v2, v2, v42
	v_add_f32_e32 v3, v3, v43
	v_add_f32_e32 v4, v4, v44
	v_lshrrev_b32_e32 v18, 3, v18
	v_max_f32_e32 v14, 0, v14
	v_max_f32_e32 v15, 0, v15
	v_max_f32_e32 v16, 0, v16
	v_add_f32_e32 v17, v17, v45
	v_max_f32_e32 v10, 0, v10
	v_max_f32_e32 v11, 0, v11
	v_max_f32_e32 v12, 0, v12
	v_add_f32_e32 v13, v13, v45
	v_max_f32_e32 v2, 0, v2
	v_max_f32_e32 v3, 0, v3
	v_max_f32_e32 v4, 0, v4
	v_add_f32_e32 v5, v5, v45
	v_max_f32_e32 v17, 0, v17
	v_cvt_pk_bf16_f32 v14, v14, v15
	v_cvt_pk_bf16_f32 v15, v16, v17
	v_xor_b32_e32 v16, v18, v118
	v_max_f32_e32 v13, 0, v13
	v_cvt_pk_bf16_f32 v10, v10, v11
	v_cvt_pk_bf16_f32 v11, v12, v13
	v_bitop3_b32 v12, v18, v70, 31 bitop3:0x78
	v_max_f32_e32 v5, 0, v5
	v_cvt_pk_bf16_f32 v2, v2, v3
	v_cvt_pk_bf16_f32 v3, v4, v5
	v_bitop3_b32 v4, v18, v71, 31 bitop3:0x78
	v_lshlrev_b32_e32 v16, 4, v16
	v_lshlrev_b32_e32 v12, 4, v12
	v_add_f32_e32 v6, v6, v42
	v_add_f32_e32 v7, v7, v43
	v_lshlrev_b32_e32 v4, 4, v4
	v_add3_u32 v16, v69, v16, v68
	v_add3_u32 v12, v72, v12, v68
	v_max_f32_e32 v6, 0, v6
	v_max_f32_e32 v7, 0, v7
	v_add_f32_e32 v8, v8, v44
	v_add_f32_e32 v9, v9, v45
	v_add3_u32 v4, v73, v4, v68
	ds_write_b64 v16, v[14:15]
	ds_write_b64 v12, v[10:11]
	v_max_f32_e32 v8, 0, v8
	v_max_f32_e32 v9, 0, v9
	v_cvt_pk_bf16_f32 v6, v6, v7
	v_cvt_pk_bf16_f32 v7, v8, v9
	ds_write_b64 v16, v[6:7] offset:16384
	ds_write_b64 v4, v[2:3]
	v_and_b32_e32 v2, 0x1f0, v1
	v_mov_b32_e32 v3, 0
	v_lshl_add_u64 v[2:3], s[0:1], 0, v[2:3]
	s_mov_b64 s[0:1], 0x2000000
	v_ashrrev_i32_e32 v6, 5, v0
	v_lshl_add_u64 v[10:11], v[2:3], 0, s[0:1]
	v_xor_b32_e32 v2, v6, v0
	v_lshlrev_b32_e32 v2, 4, v2
	v_lshlrev_b32_e32 v1, 9, v6
	v_and_b32_e32 v2, 0x1f0, v2
	v_add3_u32 v1, 0, v1, v2
	s_waitcnt lgkmcnt(0)
	s_barrier
	ds_read_b128 v[2:5], v1
	v_ashrrev_i32_e32 v7, 31, v6
	v_add_u32_e32 v1, 0x200, v0
	v_lshlrev_b64 v[6:7], 11, v[6:7]
	v_ashrrev_i32_e32 v14, 5, v1
	v_lshl_add_u64 v[12:13], v[10:11], 0, v[6:7]
	v_xor_b32_e32 v6, v14, v0
	v_lshlrev_b32_e32 v6, 4, v6
	v_lshlrev_b32_e32 v1, 9, v14
	v_and_b32_e32 v6, 0x1f0, v6
	v_add3_u32 v1, 0, v1, v6
	ds_read_b128 v[6:9], v1
	v_ashrrev_i32_e32 v15, 31, v14
	s_waitcnt lgkmcnt(1)
	global_store_dwordx4 v[12:13], v[2:5], off sc1
	v_add_u32_e32 v1, 0x400, v0
	s_nop 0
	v_lshlrev_b64 v[2:3], 11, v[14:15]
	v_lshl_add_u64 v[2:3], v[10:11], 0, v[2:3]
	s_waitcnt lgkmcnt(0)
	global_store_dwordx4 v[2:3], v[6:9], off sc1
	s_nop 1
	v_ashrrev_i32_e32 v6, 5, v1
	v_xor_b32_e32 v2, v6, v0
	v_lshlrev_b32_e32 v2, 4, v2
	v_lshlrev_b32_e32 v1, 9, v6
	v_and_b32_e32 v2, 0x1f0, v2
	v_add3_u32 v1, 0, v1, v2
	ds_read_b128 v[2:5], v1
	v_ashrrev_i32_e32 v7, 31, v6
	v_add_u32_e32 v1, 0x600, v0
	v_lshlrev_b64 v[6:7], 11, v[6:7]
	v_ashrrev_i32_e32 v14, 5, v1
	v_lshl_add_u64 v[12:13], v[10:11], 0, v[6:7]
	v_xor_b32_e32 v6, v14, v0
	v_lshlrev_b32_e32 v6, 4, v6
	v_lshlrev_b32_e32 v1, 9, v14
	v_and_b32_e32 v6, 0x1f0, v6
	v_add3_u32 v1, 0, v1, v6
	ds_read_b128 v[6:9], v1
	v_ashrrev_i32_e32 v15, 31, v14
	s_waitcnt lgkmcnt(1)
	global_store_dwordx4 v[12:13], v[2:5], off sc1
	v_add_u32_e32 v1, 0x800, v0
	s_nop 0
	v_lshlrev_b64 v[2:3], 11, v[14:15]
	v_lshl_add_u64 v[2:3], v[10:11], 0, v[2:3]
	s_waitcnt lgkmcnt(0)
	global_store_dwordx4 v[2:3], v[6:9], off sc1
	s_nop 1
	v_ashrrev_i32_e32 v6, 5, v1
	v_xor_b32_e32 v2, v6, v0
	v_lshlrev_b32_e32 v2, 4, v2
	v_lshlrev_b32_e32 v1, 9, v6
	v_and_b32_e32 v2, 0x1f0, v2
	v_add3_u32 v1, 0, v1, v2
	ds_read_b128 v[2:5], v1
	v_ashrrev_i32_e32 v7, 31, v6
	v_add_u32_e32 v1, 0xa00, v0
	v_lshlrev_b64 v[6:7], 11, v[6:7]
	v_ashrrev_i32_e32 v14, 5, v1
	v_lshl_add_u64 v[12:13], v[10:11], 0, v[6:7]
	v_xor_b32_e32 v6, v14, v0
	v_lshlrev_b32_e32 v6, 4, v6
	v_lshlrev_b32_e32 v1, 9, v14
	v_and_b32_e32 v6, 0x1f0, v6
	v_add3_u32 v1, 0, v1, v6
	ds_read_b128 v[6:9], v1
	v_ashrrev_i32_e32 v15, 31, v14
	s_waitcnt lgkmcnt(1)
	global_store_dwordx4 v[12:13], v[2:5], off sc1
	v_add_u32_e32 v1, 0xc00, v0
	s_nop 0
	v_lshlrev_b64 v[2:3], 11, v[14:15]
	v_lshl_add_u64 v[2:3], v[10:11], 0, v[2:3]
	s_waitcnt lgkmcnt(0)
	global_store_dwordx4 v[2:3], v[6:9], off sc1
	s_nop 1
	v_ashrrev_i32_e32 v6, 5, v1
	v_xor_b32_e32 v2, v6, v0
	v_lshlrev_b32_e32 v2, 4, v2
	v_lshlrev_b32_e32 v1, 9, v6
	v_and_b32_e32 v2, 0x1f0, v2
	v_add3_u32 v1, 0, v1, v2
	ds_read_b128 v[2:5], v1
	v_add_u32_e32 v1, 0xe00, v0
	v_ashrrev_i32_e32 v14, 5, v1
	v_xor_b32_e32 v0, v14, v0
	v_lshlrev_b32_e32 v0, 4, v0
	v_ashrrev_i32_e32 v7, 31, v6
	v_lshlrev_b32_e32 v1, 9, v14
	v_and_b32_e32 v0, 0x1f0, v0
	v_lshlrev_b64 v[6:7], 11, v[6:7]
	v_add3_u32 v0, 0, v1, v0
	v_lshl_add_u64 v[12:13], v[10:11], 0, v[6:7]
	ds_read_b128 v[6:9], v0
	v_ashrrev_i32_e32 v15, 31, v14
	v_lshlrev_b64 v[0:1], 11, v[14:15]
	v_lshl_add_u64 v[0:1], v[10:11], 0, v[0:1]
	s_waitcnt lgkmcnt(1)
	global_store_dwordx4 v[12:13], v[2:5], off sc1
	s_waitcnt lgkmcnt(0)
	global_store_dwordx4 v[0:1], v[6:9], off sc1
	s_endpgm
.Lrot1_loop:
	s_and_b32 s0, s29, 0x10000
	v_add_u32_e32 v211, s0, v209
	v_add_u32_e32 v242, s0, v210
	s_xor_b32 s0, s0, 0x10000
	s_and_b32 s1, s22, 0x3c0
	s_add_i32 s23, s0, 0
	s_lshl_b32 s0, s1, 2
	s_add_u32 s20, s25, s0
	s_waitcnt vmcnt(10)
	v_cvt_pk_bf16_f32 v46, v46, v47
	v_cvt_pk_bf16_f32 v47, v48, v49
	v_cvt_pk_bf16_f32 v48, v42, v43
	v_cvt_pk_bf16_f32 v49, v44, v45
	s_waitcnt vmcnt(8)
	v_cvt_pk_bf16_f32 v38, v38, v39
	v_cvt_pk_bf16_f32 v39, v40, v41
	v_cvt_pk_bf16_f32 v40, v34, v35
	v_add_u32_e32 v34, s23, v208
	s_addc_u32 s21, s26, 0
	s_lshl_b32 s0, s1, 1
	v_cvt_pk_bf16_f32 v41, v36, v37
	v_lshlrev_b32_e32 v182, 2, v178
	v_add_u32_e32 v35, s23, v205
	v_add_u32_e32 v36, s23, v206
	v_add_u32_e32 v37, s23, v207
	ds_write_b128 v34, v[46:49]
	ds_write_b128 v35, v[38:41]
	s_waitcnt vmcnt(7)
	ds_write_b128 v36, v[30:33] offset:32768
	s_waitcnt vmcnt(6)
	ds_write_b128 v37, v[26:29] offset:32768
	v_lshl_add_u64 v[26:27], s[20:21], 0, v[180:181]
	v_lshl_add_u64 v[28:29], s[20:21], 0, v[184:185]
	s_add_u32 s0, s27, s0
	v_lshl_add_u64 v[26:27], v[26:27], 0, v[182:183]
	v_lshl_add_u64 v[28:29], v[28:29], 0, v[182:183]
	s_addc_u32 s1, s28, 0
	v_lshlrev_b32_e32 v240, 1, v178
	v_mov_b32_e32 v241, v183
	global_load_dwordx4 v[42:45], v[26:27], off offset:16
	global_load_dwordx4 v[46:49], v[26:27], off
	global_load_dwordx4 v[34:37], v[28:29], off offset:16
	global_load_dwordx4 v[38:41], v[28:29], off
	v_lshl_add_u64 v[26:27], s[0:1], 0, v[186:187]
	v_lshl_add_u64 v[28:29], s[0:1], 0, v[188:189]
	v_lshl_add_u64 v[26:27], v[26:27], 0, v[240:241]
	v_lshl_add_u64 v[28:29], v[28:29], 0, v[240:241]
	global_load_dwordx4 v[30:33], v[26:27], off
	s_nop 0
	global_load_dwordx4 v[26:29], v[28:29], off
	ds_read_b128 v[212:215], v242 offset:0
	ds_read_b128 v[216:219], v242 offset:0x800
	ds_read_b128 v[220:223], v242 offset:0x1000
	ds_read_b128 v[224:227], v242 offset:0x1800
	ds_read_b128 v[228:231], v211 offset:0
	ds_read_b128 v[232:235], v211 offset:0x800
	ds_read_b128 v[236:239], v211 offset:0x1000
	s_waitcnt lgkmcnt(2)
	v_mfma_f32_16x16x32_bf16 v[174:177], v[212:215], v[228:231], v[174:177]
	v_mfma_f32_16x16x32_bf16 v[170:173], v[216:219], v[228:231], v[170:173]
	v_mfma_f32_16x16x32_bf16 v[166:169], v[220:223], v[228:231], v[166:169]
	v_mfma_f32_16x16x32_bf16 v[162:165], v[224:227], v[228:231], v[162:165]
	ds_read_b128 v[228:231], v211 offset:0x1800
	s_waitcnt lgkmcnt(2)
	v_mfma_f32_16x16x32_bf16 v[158:161], v[212:215], v[232:235], v[158:161]
	v_mfma_f32_16x16x32_bf16 v[154:157], v[216:219], v[232:235], v[154:157]
	v_mfma_f32_16x16x32_bf16 v[150:153], v[220:223], v[232:235], v[150:153]
	v_mfma_f32_16x16x32_bf16 v[146:149], v[224:227], v[232:235], v[146:149]
	ds_read_b128 v[232:235], v211 offset:0x2000
	s_waitcnt lgkmcnt(2)
	v_mfma_f32_16x16x32_bf16 v[142:145], v[212:215], v[236:239], v[142:145]
	v_mfma_f32_16x16x32_bf16 v[138:141], v[216:219], v[236:239], v[138:141]
	v_mfma_f32_16x16x32_bf16 v[134:137], v[220:223], v[236:239], v[134:137]
	v_mfma_f32_16x16x32_bf16 v[130:133], v[224:227], v[236:239], v[130:133]
	ds_read_b128 v[236:239], v211 offset:0x2800
	s_waitcnt lgkmcnt(2)
	v_mfma_f32_16x16x32_bf16 v[126:129], v[212:215], v[228:231], v[126:129]
	v_mfma_f32_16x16x32_bf16 v[122:125], v[216:219], v[228:231], v[122:125]
	v_mfma_f32_16x16x32_bf16 v[118:121], v[220:223], v[228:231], v[118:121]
	v_mfma_f32_16x16x32_bf16 v[114:117], v[224:227], v[228:231], v[114:117]
	ds_read_b128 v[228:231], v211 offset:0x3000
	s_waitcnt lgkmcnt(2)
	v_mfma_f32_16x16x32_bf16 v[110:113], v[212:215], v[232:235], v[110:113]
	v_mfma_f32_16x16x32_bf16 v[106:109], v[216:219], v[232:235], v[106:109]
	v_mfma_f32_16x16x32_bf16 v[102:105], v[220:223], v[232:235], v[102:105]
	v_mfma_f32_16x16x32_bf16 v[98:101], v[224:227], v[232:235], v[98:101]
	ds_read_b128 v[232:235], v211 offset:0x3800
	s_waitcnt lgkmcnt(2)
	v_mfma_f32_16x16x32_bf16 v[94:97], v[212:215], v[236:239], v[94:97]
	v_mfma_f32_16x16x32_bf16 v[90:93], v[216:219], v[236:239], v[90:93]
	v_mfma_f32_16x16x32_bf16 v[86:89], v[220:223], v[236:239], v[86:89]
	v_mfma_f32_16x16x32_bf16 v[82:85], v[224:227], v[236:239], v[82:85]
	s_waitcnt lgkmcnt(1)
	v_mfma_f32_16x16x32_bf16 v[78:81], v[212:215], v[228:231], v[78:81]
	v_mfma_f32_16x16x32_bf16 v[74:77], v[216:219], v[228:231], v[74:77]
	v_mfma_f32_16x16x32_bf16 v[70:73], v[220:223], v[228:231], v[70:73]
	v_mfma_f32_16x16x32_bf16 v[66:69], v[224:227], v[228:231], v[66:69]
	s_waitcnt lgkmcnt(0)
	v_mfma_f32_16x16x32_bf16 v[62:65], v[212:215], v[232:235], v[62:65]
	v_mfma_f32_16x16x32_bf16 v[58:61], v[216:219], v[232:235], v[58:61]
	v_mfma_f32_16x16x32_bf16 v[54:57], v[220:223], v[232:235], v[54:57]
	v_mfma_f32_16x16x32_bf16 v[50:53], v[224:227], v[232:235], v[50:53]
	s_waitcnt vmcnt(10)
	v_cvt_pk_bf16_f32 v22, v22, v23
	v_cvt_pk_bf16_f32 v23, v24, v25
	v_cvt_pk_bf16_f32 v24, v6, v7
	v_cvt_pk_bf16_f32 v25, v8, v9
	v_add_u32_e32 v6, s23, v204
	s_waitcnt vmcnt(9)
	v_cvt_pk_bf16_f32 v8, v2, v3
	v_add_u32_e32 v2, s23, v201
	ds_write_b128 v6, v[22:25]
	s_waitcnt vmcnt(8)
	v_cvt_pk_bf16_f32 v6, v10, v11
	v_cvt_pk_bf16_f32 v7, v12, v13
	v_cvt_pk_bf16_f32 v9, v4, v5
	ds_write_b128 v2, v[6:9]
	v_add_u32_e32 v2, s23, v202
	s_waitcnt vmcnt(7)
	ds_write_b128 v2, v[18:21] offset:32768
	v_add_u32_e32 v2, s23, v203
	s_waitcnt vmcnt(6)
	ds_write_b128 v2, v[14:17] offset:32768
	v_lshl_add_u64 v[2:3], s[20:21], 0, v[190:191]
	v_lshl_add_u64 v[2:3], v[2:3], 0, v[182:183]
	global_load_dwordx4 v[6:9], v[2:3], off offset:16
	global_load_dwordx4 v[22:25], v[2:3], off
	v_lshl_add_u64 v[2:3], s[20:21], 0, v[192:193]
	v_lshl_add_u64 v[14:15], s[0:1], 0, v[194:195]
	v_lshl_add_u64 v[16:17], s[0:1], 0, v[196:197]
	v_lshl_add_u64 v[10:11], v[2:3], 0, v[182:183]
	v_lshl_add_u64 v[14:15], v[14:15], 0, v[240:241]
	v_lshl_add_u64 v[16:17], v[16:17], 0, v[240:241]
	global_load_dwordx4 v[2:5], v[10:11], off offset:16
	s_nop 0
	global_load_dwordx4 v[10:13], v[10:11], off
	s_nop 0
	global_load_dwordx4 v[18:21], v[14:15], off
	s_nop 0
	global_load_dwordx4 v[14:17], v[16:17], off
	ds_read_b128 v[212:215], v242 offset:0x400
	ds_read_b128 v[216:219], v242 offset:0xc00
	ds_read_b128 v[220:223], v242 offset:0x1400
	ds_read_b128 v[224:227], v242 offset:0x1c00
	ds_read_b128 v[228:231], v211 offset:0x400
	ds_read_b128 v[232:235], v211 offset:0xc00
	ds_read_b128 v[236:239], v211 offset:0x1400
	s_waitcnt lgkmcnt(2)
	v_mfma_f32_16x16x32_bf16 v[174:177], v[212:215], v[228:231], v[174:177]
	v_mfma_f32_16x16x32_bf16 v[170:173], v[216:219], v[228:231], v[170:173]
	v_mfma_f32_16x16x32_bf16 v[166:169], v[220:223], v[228:231], v[166:169]
	v_mfma_f32_16x16x32_bf16 v[162:165], v[224:227], v[228:231], v[162:165]
	ds_read_b128 v[228:231], v211 offset:0x1c00
	s_waitcnt lgkmcnt(2)
	v_mfma_f32_16x16x32_bf16 v[158:161], v[212:215], v[232:235], v[158:161]
	v_mfma_f32_16x16x32_bf16 v[154:157], v[216:219], v[232:235], v[154:157]
	v_mfma_f32_16x16x32_bf16 v[150:153], v[220:223], v[232:235], v[150:153]
	v_mfma_f32_16x16x32_bf16 v[146:149], v[224:227], v[232:235], v[146:149]
	ds_read_b128 v[232:235], v211 offset:0x2400
	s_waitcnt lgkmcnt(2)
	v_mfma_f32_16x16x32_bf16 v[142:145], v[212:215], v[236:239], v[142:145]
	v_mfma_f32_16x16x32_bf16 v[138:141], v[216:219], v[236:239], v[138:141]
	v_mfma_f32_16x16x32_bf16 v[134:137], v[220:223], v[236:239], v[134:137]
	v_mfma_f32_16x16x32_bf16 v[130:133], v[224:227], v[236:239], v[130:133]
	ds_read_b128 v[236:239], v211 offset:0x2c00
	s_waitcnt lgkmcnt(2)
	v_mfma_f32_16x16x32_bf16 v[126:129], v[212:215], v[228:231], v[126:129]
	v_mfma_f32_16x16x32_bf16 v[122:125], v[216:219], v[228:231], v[122:125]
	v_mfma_f32_16x16x32_bf16 v[118:121], v[220:223], v[228:231], v[118:121]
	v_mfma_f32_16x16x32_bf16 v[114:117], v[224:227], v[228:231], v[114:117]
	ds_read_b128 v[228:231], v211 offset:0x3400
	s_waitcnt lgkmcnt(2)
	v_mfma_f32_16x16x32_bf16 v[110:113], v[212:215], v[232:235], v[110:113]
	v_mfma_f32_16x16x32_bf16 v[106:109], v[216:219], v[232:235], v[106:109]
	v_mfma_f32_16x16x32_bf16 v[102:105], v[220:223], v[232:235], v[102:105]
	v_mfma_f32_16x16x32_bf16 v[98:101], v[224:227], v[232:235], v[98:101]
	ds_read_b128 v[232:235], v211 offset:0x3c00
	s_waitcnt lgkmcnt(2)
	v_mfma_f32_16x16x32_bf16 v[94:97], v[212:215], v[236:239], v[94:97]
	v_mfma_f32_16x16x32_bf16 v[90:93], v[216:219], v[236:239], v[90:93]
	v_mfma_f32_16x16x32_bf16 v[86:89], v[220:223], v[236:239], v[86:89]
	v_mfma_f32_16x16x32_bf16 v[82:85], v[224:227], v[236:239], v[82:85]
	s_waitcnt lgkmcnt(1)
	v_mfma_f32_16x16x32_bf16 v[78:81], v[212:215], v[228:231], v[78:81]
	v_mfma_f32_16x16x32_bf16 v[74:77], v[216:219], v[228:231], v[74:77]
	v_mfma_f32_16x16x32_bf16 v[70:73], v[220:223], v[228:231], v[70:73]
	v_mfma_f32_16x16x32_bf16 v[66:69], v[224:227], v[228:231], v[66:69]
	s_waitcnt lgkmcnt(0)
	v_mfma_f32_16x16x32_bf16 v[62:65], v[212:215], v[232:235], v[62:65]
	v_mfma_f32_16x16x32_bf16 v[58:61], v[216:219], v[232:235], v[58:61]
	v_mfma_f32_16x16x32_bf16 v[54:57], v[220:223], v[232:235], v[54:57]
	v_mfma_f32_16x16x32_bf16 v[50:53], v[224:227], v[232:235], v[50:53]
	s_waitcnt lgkmcnt(0)
	s_add_i32 s22, s22, 64
	s_add_i32 s29, s29, 0x10000
	s_cmp_lg_u32 s29, 0xe0000
	s_barrier
	s_cbranch_scc1 .Lrot1_loop
	s_branch .Lrot1_done
.Lrot2_loop:
	s_and_b32 s0, s3, 0x10000
	v_add_u32_e32 v158, s0, v128
	v_add_u32_e32 v159, s0, v129
	s_xor_b32 s0, s0, 0x10000
	s_and_b32 s6, s2, 0x3c0
	s_add_i32 s14, s0, 0
	s_lshl_b32 s0, s6, 2
	s_lshl_b32 s6, s6, 1
	s_add_u32 s6, s12, s6
	s_waitcnt vmcnt(6)
	v_cvt_pk_bf16_f32 v34, v34, v35
	v_cvt_pk_bf16_f32 v35, v36, v37
	v_cvt_pk_bf16_f32 v36, v30, v31
	v_cvt_pk_bf16_f32 v37, v32, v33
	v_add_u32_e32 v30, s14, v125
	s_addc_u32 s7, s13, 0
	v_add_u32_e32 v31, s14, v126
	v_add_u32_e32 v32, s14, v127
	ds_write_b128 v30, v[34:37]
	s_waitcnt vmcnt(5)
	ds_write_b128 v31, v[26:29] offset:32768
	s_waitcnt vmcnt(4)
	ds_write_b128 v32, v[22:25] offset:32768
	v_lshl_add_u64 v[22:23], s[6:7], 0, v[102:103]
	v_lshl_add_u64 v[24:25], s[6:7], 0, v[104:105]
	v_lshl_add_u64 v[130:131], v[114:115], 0, s[0:1]
	v_lshl_add_u64 v[22:23], v[98:99], 1, v[22:23]
	v_lshl_add_u64 v[24:25], v[100:101], 1, v[24:25]
	global_load_dwordx4 v[30:33], v[130:131], off offset:16
	global_load_dwordx4 v[34:37], v[130:131], off
	global_load_dwordx4 v[26:29], v[22:23], off
	s_nop 0
	global_load_dwordx4 v[22:25], v[24:25], off
	ds_read_b128 v[130:133], v159 offset:0
	ds_read_b128 v[134:137], v159 offset:0x800
	ds_read_b128 v[138:141], v159 offset:0x1000
	ds_read_b128 v[142:145], v159 offset:0x1800
	ds_read_b128 v[146:149], v158 offset:0
	ds_read_b128 v[150:153], v158 offset:0x800
	ds_read_b128 v[154:157], v158 offset:0x1000
	s_waitcnt lgkmcnt(2)
	v_mfma_f32_16x16x32_bf16 v[94:97], v[130:133], v[146:149], v[94:97]
	v_mfma_f32_16x16x32_bf16 v[90:93], v[134:137], v[146:149], v[90:93]
	v_mfma_f32_16x16x32_bf16 v[86:89], v[138:141], v[146:149], v[86:89]
	v_mfma_f32_16x16x32_bf16 v[82:85], v[142:145], v[146:149], v[82:85]
	ds_read_b128 v[146:149], v158 offset:0x1800
	s_waitcnt lgkmcnt(2)
	v_mfma_f32_16x16x32_bf16 v[78:81], v[130:133], v[150:153], v[78:81]
	v_mfma_f32_16x16x32_bf16 v[74:77], v[134:137], v[150:153], v[74:77]
	v_mfma_f32_16x16x32_bf16 v[70:73], v[138:141], v[150:153], v[70:73]
	v_mfma_f32_16x16x32_bf16 v[66:69], v[142:145], v[150:153], v[66:69]
	s_waitcnt lgkmcnt(1)
	v_mfma_f32_16x16x32_bf16 v[62:65], v[130:133], v[154:157], v[62:65]
	v_mfma_f32_16x16x32_bf16 v[58:61], v[134:137], v[154:157], v[58:61]
	v_mfma_f32_16x16x32_bf16 v[54:57], v[138:141], v[154:157], v[54:57]
	v_mfma_f32_16x16x32_bf16 v[50:53], v[142:145], v[154:157], v[50:53]
	s_waitcnt lgkmcnt(0)
	v_mfma_f32_16x16x32_bf16 v[46:49], v[130:133], v[146:149], v[46:49]
	v_mfma_f32_16x16x32_bf16 v[42:45], v[134:137], v[146:149], v[42:45]
	v_mfma_f32_16x16x32_bf16 v[38:41], v[138:141], v[146:149], v[38:41]
	v_mfma_f32_16x16x32_bf16 v[2:5], v[142:145], v[146:149], v[2:5]
	v_add_u32_e32 v130, s14, v122
	s_waitcnt vmcnt(6)
	v_cvt_pk_bf16_f32 v10, v10, v11
	v_cvt_pk_bf16_f32 v11, v12, v13
	v_cvt_pk_bf16_f32 v12, v6, v7
	v_add_u32_e32 v6, s14, v123
	v_cvt_pk_bf16_f32 v13, v8, v9
	ds_write_b128 v130, v[10:13]
	s_waitcnt vmcnt(5)
	ds_write_b128 v6, v[18:21] offset:32768
	v_add_u32_e32 v6, s14, v124
	s_waitcnt vmcnt(4)
	ds_write_b128 v6, v[14:17] offset:32768
	v_lshl_add_u64 v[14:15], s[6:7], 0, v[110:111]
	v_lshl_add_u64 v[16:17], s[6:7], 0, v[112:113]
	v_lshl_add_u64 v[10:11], v[116:117], 0, s[0:1]
	v_lshl_add_u64 v[14:15], v[106:107], 1, v[14:15]
	v_lshl_add_u64 v[16:17], v[108:109], 1, v[16:17]
	global_load_dwordx4 v[6:9], v[10:11], off offset:16
	s_nop 0
	global_load_dwordx4 v[10:13], v[10:11], off
	s_nop 0
	global_load_dwordx4 v[18:21], v[14:15], off
	s_nop 0
	global_load_dwordx4 v[14:17], v[16:17], off
	ds_read_b128 v[130:133], v159 offset:0x400
	ds_read_b128 v[134:137], v159 offset:0xc00
	ds_read_b128 v[138:141], v159 offset:0x1400
	ds_read_b128 v[142:145], v159 offset:0x1c00
	ds_read_b128 v[146:149], v158 offset:0x400
	ds_read_b128 v[150:153], v158 offset:0xc00
	ds_read_b128 v[154:157], v158 offset:0x1400
	s_waitcnt lgkmcnt(2)
	v_mfma_f32_16x16x32_bf16 v[94:97], v[130:133], v[146:149], v[94:97]
	v_mfma_f32_16x16x32_bf16 v[90:93], v[134:137], v[146:149], v[90:93]
	v_mfma_f32_16x16x32_bf16 v[86:89], v[138:141], v[146:149], v[86:89]
	v_mfma_f32_16x16x32_bf16 v[82:85], v[142:145], v[146:149], v[82:85]
	ds_read_b128 v[146:149], v158 offset:0x1c00
	s_waitcnt lgkmcnt(2)
	v_mfma_f32_16x16x32_bf16 v[78:81], v[130:133], v[150:153], v[78:81]
	v_mfma_f32_16x16x32_bf16 v[74:77], v[134:137], v[150:153], v[74:77]
	v_mfma_f32_16x16x32_bf16 v[70:73], v[138:141], v[150:153], v[70:73]
	v_mfma_f32_16x16x32_bf16 v[66:69], v[142:145], v[150:153], v[66:69]
	s_waitcnt lgkmcnt(1)
	v_mfma_f32_16x16x32_bf16 v[62:65], v[130:133], v[154:157], v[62:65]
	v_mfma_f32_16x16x32_bf16 v[58:61], v[134:137], v[154:157], v[58:61]
	v_mfma_f32_16x16x32_bf16 v[54:57], v[138:141], v[154:157], v[54:57]
	v_mfma_f32_16x16x32_bf16 v[50:53], v[142:145], v[154:157], v[50:53]
	s_waitcnt lgkmcnt(0)
	v_mfma_f32_16x16x32_bf16 v[46:49], v[130:133], v[146:149], v[46:49]
	v_mfma_f32_16x16x32_bf16 v[42:45], v[134:137], v[146:149], v[42:45]
	v_mfma_f32_16x16x32_bf16 v[38:41], v[138:141], v[146:149], v[38:41]
	v_mfma_f32_16x16x32_bf16 v[2:5], v[142:145], v[146:149], v[2:5]
	s_waitcnt lgkmcnt(0)
	s_add_i32 s2, s2, 64
	s_add_i32 s3, s3, 0x10000
	s_cmp_lg_u32 s3, 0xe0000
	s_barrier
	s_cbranch_scc1 .Lrot2_loop
	s_branch .Lrot2_done
